# instruction selection: hipcc's f32->bf16 round-to-nearest-even bit-trick sequences (v_bfe/v_add3/v_lshrrev/v_and_or) replaced by v_cvt_pk_bf16_f32 at 101 sites (bit-identical for non-NaN inputs; denor
# baseline (speedup 1.0000x reference)
; __device__ __forceinline__ unsigned pk2(float lo, float hi) { return f2bf(lo) | (f2bf(hi) << 16); }
; __device__ __forceinline__ float dpp_x1(float v) { return __builtin_bit_cast(float, __builtin_amdgcn_update_dpp(0, __builtin_bit_cast(int, v), 0xB1, 0xF, 0xF, true)); }
; __device__ __forceinline__ float dpp_x2(float v) { return __builtin_bit_cast(float, __builtin_amdgcn_update_dpp(0, __builtin_bit_cast(int, v), 0x4E, 0xF, 0xF, true)); }
; __device__ __forceinline__ float dpp_hm(float v) { return __builtin_bit_cast(float, __builtin_amdgcn_update_dpp(0, __builtin_bit_cast(int, v), 0x141, 0xF, 0xF, true)); }
; __device__ __forceinline__ void qk_vec(bf16_t* p, const u32x4 r, const float (&w)[8], const float (&cs)[8], const float (&sn)[8]) {
;     float x[8] = {bflo(r.x), bfhi(r.x), bflo(r.y), bfhi(r.y), bflo(r.z), bfhi(r.z), bflo(r.w), bfhi(r.w)};
;     float ss = 0.f;
; #pragma unroll
;     for (int e = 0; e < 8; ++e) ss += x[e] * x[e];
;     ss += dpp_x1(ss); ss += dpp_x2(ss); ss += dpp_hm(ss);
;     const float rstd = rsqrtf(ss * (1.f / 64.f) + NORM_EPS);
;     float o[8];
; #pragma unroll
;     for (int e = 0; e < 8; ++e) { const float y = x[e] * rstd * w[e]; o[e] = y * cs[e] + dpp_x2(y) * sn[e]; }
;     u32x4 q; q.x = pk2(o[0], o[1]); q.y = pk2(o[2], o[3]); q.z = pk2(o[4], o[5]); q.w = pk2(o[6], o[7]);
;     *(u32x4*)p = q;
; }
; __device__ __forceinline__ void prep_qk_rows4(KP Pk, Frame& F, int l, int row0) {
;     ...
;     for (int r = 0; r < 4; ++r) { bf16_t* up = U + (size_t)(row0 + r) * NU + 8 * F.lane;
;         qk_vec(up + UC_SQ, raw[r][0], wsq, cs[r], sn[r]); qk_vec(up + UC_DQ, raw[r][1], wdq, cs[r], sn[r]); qk_vec(up + UC_DK, raw[r][2], wdk, cs[r], sn[r]); }
.LBB0_385:
	s_or_b64 exec, exec, s[8:9]
	s_mov_b64 s[8:9], 0x1e00
	v_lshl_add_u64 v[224:225], v[198:199], 0, s[8:9]
	v_lshl_add_u64 v[220:221], v[162:163], 0, s[8:9]
	v_lshl_add_u64 v[216:217], v[134:135], 0, s[8:9]
	v_lshl_add_u64 v[178:179], v[132:133], 0, s[8:9]
	s_mov_b64 s[8:9], 0x1000
	v_lshl_add_u64 v[160:161], v[160:161], 0, s[8:9]
	s_mov_b32 s8, 0x3e38aa3b
	s_waitcnt vmcnt(0)
	v_mov_b32_e32 v16, v107
	v_mov_b32_e32 v20, v103
	v_mov_b32_e32 v21, v105
	v_mov_b32_e32 v107, v108
	v_mov_b32_e32 v12, v111
	v_mov_b32_e32 v13, v113
	v_mov_b32_e32 v111, v112
	v_pk_mul_f32 v[112:113], v[20:21], s[8:9] op_sel_hi:[1,0]
	v_pk_mul_f32 v[20:21], v[106:107], s[8:9] op_sel_hi:[1,0]
	v_lshlrev_b32_e32 v106, 16, v98
	v_and_b32_e32 v108, 0xffff0000, v98
	v_mov_b32_e32 v8, v115
	v_mov_b32_e32 v115, v116
	v_mov_b32_e32 v17, v109
	v_lshlrev_b32_e32 v107, 16, v99
	v_and_b32_e32 v109, 0xffff0000, v99
	v_mov_b32_e32 v98, v106
	v_mov_b32_e32 v99, v108
	v_pk_mul_f32 v[196:197], v[12:13], s[8:9] op_sel_hi:[1,0]
	v_pk_mul_f32 v[12:13], v[114:115], s[8:9] op_sel_hi:[1,0]
	v_pk_mul_f32 v[98:99], v[98:99], v[98:99]
	v_mov_b32_e32 v114, v109
	v_mov_b32_e32 v115, v107
	v_pk_mul_f32 v[114:115], v[114:115], v[114:115]
	v_lshlrev_b32_e32 v116, 16, v100
	v_and_b32_e32 v100, 0xffff0000, v100
	v_add_f32_e32 v67, v98, v99
	v_mov_b32_e32 v242, v100
	v_mov_b32_e32 v243, v116
	v_add_f32_e32 v67, v115, v67
	v_mov_b32_e32 v9, v117
	v_lshlrev_b32_e32 v117, 16, v101
	v_and_b32_e32 v101, 0xffff0000, v101
	v_pk_mul_f32 v[242:243], v[242:243], v[242:243]
	v_add_f32_e32 v67, v114, v67
	v_mov_b32_e32 v244, v101
	v_mov_b32_e32 v245, v117
	v_add_f32_e32 v67, v243, v67
	v_pk_mul_f32 v[244:245], v[244:245], v[244:245]
	v_add_f32_e32 v67, v242, v67
	v_add_f32_e32 v67, v245, v67
	v_add_f32_e32 v67, v244, v67
	v_mov_b32_e32 v103, v104
	v_pk_mul_f32 v[98:99], v[102:103], s[8:9] op_sel_hi:[1,0]
	v_add_f32_dpp v67, v67, v67 quad_perm:[1,0,3,2] row_mask:0xf bank_mask:0xf bound_ctrl:1
	v_pk_mul_f32 v[110:111], v[110:111], s[8:9] op_sel_hi:[1,0]
	s_mov_b64 s[18:19], 0x2200
	v_add_f32_dpp v67, v67, v67 quad_perm:[2,3,0,1] row_mask:0xf bank_mask:0xf bound_ctrl:1
	v_lshl_add_u64 v[222:223], v[198:199], 0, s[18:19]
	v_and_b32_e32 v244, 0xffff0000, v92
	v_add_f32_dpp v67, v67, v67 row_half_mirror row_mask:0xf bank_mask:0xf bound_ctrl:1
	v_fmamk_f32 v67, v67, 0x3c800000, v194
	v_mul_f32_e32 v69, 0x4b800000, v67
	v_cmp_gt_f32_e32 vcc, s66, v67
	v_and_b32_e32 v245, 0xffff0000, v93
	v_mov_b32_e32 v250, v245
	v_cndmask_b32_e32 v67, v67, v69, vcc
	v_rsq_f32_e32 v67, v67
	v_pk_mul_f32 v[8:9], v[8:9], s[8:9] op_sel_hi:[1,0]
	v_pk_mul_f32 v[16:17], v[16:17], s[8:9] op_sel_hi:[1,0]
	s_mov_b32 s8, 0x358637bd
	v_mul_f32_e32 v69, 0x45800000, v67
	v_cndmask_b32_e32 v102, v67, v69, vcc
	v_pk_mul_f32 v[104:105], v[102:103], v[106:107] op_sel_hi:[0,1]
	v_pk_mul_f32 v[104:105], v[98:99], v[104:105]
	v_pk_mul_f32 v[108:109], v[102:103], v[108:109] op_sel_hi:[0,1]
	v_pk_mul_f32 v[108:109], v[112:113], v[108:109]
	v_mov_b32_dpp v106, v104 quad_perm:[2,3,0,1] row_mask:0xf bank_mask:0xf bound_ctrl:1
	v_pk_mul_f32 v[242:243], v[214:215], v[104:105]
	v_mov_b32_dpp v107, v105 quad_perm:[2,3,0,1] row_mask:0xf bank_mask:0xf bound_ctrl:1
	v_mov_b32_dpp v114, v108 quad_perm:[2,3,0,1] row_mask:0xf bank_mask:0xf bound_ctrl:1
	v_pk_fma_f32 v[104:105], v[206:207], v[106:107], v[242:243]
	v_pk_mul_f32 v[106:107], v[212:213], v[108:109]
	v_mov_b32_dpp v115, v109 quad_perm:[2,3,0,1] row_mask:0xf bank_mask:0xf bound_ctrl:1
	v_pk_mul_f32 v[108:109], v[102:103], v[116:117] op_sel_hi:[0,1]
	v_pk_mul_f32 v[108:109], v[110:111], v[108:109]
	v_pk_mul_f32 v[100:101], v[102:103], v[100:101] op_sel_hi:[0,1]
	v_pk_fma_f32 v[106:107], v[202:203], v[114:115], v[106:107]
	v_mov_b32_dpp v114, v108 quad_perm:[2,3,0,1] row_mask:0xf bank_mask:0xf bound_ctrl:1
	v_pk_mul_f32 v[100:101], v[196:197], v[100:101]
	v_pk_mul_f32 v[116:117], v[210:211], v[108:109]
	v_mov_b32_dpp v115, v109 quad_perm:[2,3,0,1] row_mask:0xf bank_mask:0xf bound_ctrl:1
	v_mov_b32_dpp v102, v100 quad_perm:[2,3,0,1] row_mask:0xf bank_mask:0xf bound_ctrl:1
	v_pk_fma_f32 v[108:109], v[200:201], v[114:115], v[116:117]
	v_pk_mul_f32 v[114:115], v[208:209], v[100:101]
	v_mov_b32_dpp v103, v101 quad_perm:[2,3,0,1] row_mask:0xf bank_mask:0xf bound_ctrl:1
	v_pk_fma_f32 v[100:101], v[204:205], v[102:103], v[114:115]
	v_cvt_pk_bf16_f32 v103, v109, v101
	v_cvt_pk_bf16_f32 v102, v108, v100
	v_cvt_pk_bf16_f32 v101, v105, v107
	v_cvt_pk_bf16_f32 v100, v104, v106
	global_store_dwordx4 v[198:199], v[100:103], off offset:3072
	v_lshlrev_b32_e32 v116, 16, v90
	v_and_b32_e32 v198, 0xffff0000, v90
	v_lshlrev_b32_e32 v100, 16, v94
	v_and_b32_e32 v94, 0xffff0000, v94
	v_mov_b32_e32 v102, v100
	v_mov_b32_e32 v103, v94
	v_lshlrev_b32_e32 v117, 16, v91
	v_and_b32_e32 v199, 0xffff0000, v91
	v_mov_b32_e32 v90, v116
	v_mov_b32_e32 v91, v198
	v_pk_mul_f32 v[102:103], v[102:103], v[102:103]
	v_pk_mul_f32 v[90:91], v[90:91], v[90:91]
	v_lshlrev_b32_e32 v101, 16, v95
	v_and_b32_e32 v95, 0xffff0000, v95
	v_mov_b32_e32 v242, v90
	v_mov_b32_e32 v243, v102
	v_mov_b32_e32 v102, v91
	v_mov_b32_e32 v104, v95
	v_mov_b32_e32 v105, v101
	v_pk_add_f32 v[90:91], v[242:243], v[102:103]
	v_mov_b32_e32 v102, v199
	v_mov_b32_e32 v103, v117
	v_pk_mul_f32 v[228:229], v[104:105], v[104:105]
	v_lshlrev_b32_e32 v106, 16, v96
	v_and_b32_e32 v96, 0xffff0000, v96
	v_pk_mul_f32 v[102:103], v[102:103], v[102:103]
	v_lshlrev_b32_e32 v242, 16, v92
	v_mov_b32_e32 v108, v96
	v_mov_b32_e32 v109, v106
	v_lshlrev_b32_e32 v243, 16, v93
	v_mov_b32_e32 v92, v244
	v_mov_b32_e32 v93, v242
	v_mov_b32_e32 v104, v103
	v_mov_b32_e32 v105, v229
; __device__ __forceinline__ unsigned pk2(float lo, float hi) { return f2bf(lo) | (f2bf(hi) << 16); }
; __device__ __forceinline__ float dpp_x1(float v) { return __builtin_bit_cast(float, __builtin_amdgcn_update_dpp(0, __builtin_bit_cast(int, v), 0xB1, 0xF, 0xF, true)); }
; __device__ __forceinline__ float dpp_x2(float v) { return __builtin_bit_cast(float, __builtin_amdgcn_update_dpp(0, __builtin_bit_cast(int, v), 0x4E, 0xF, 0xF, true)); }
; __device__ __forceinline__ float dpp_hm(float v) { return __builtin_bit_cast(float, __builtin_amdgcn_update_dpp(0, __builtin_bit_cast(int, v), 0x141, 0xF, 0xF, true)); }
; __device__ __forceinline__ void qk_vec(bf16_t* p, const u32x4 r, const float (&w)[8], const float (&cs)[8], const float (&sn)[8]) {
;     float x[8] = {bflo(r.x), bfhi(r.x), bflo(r.y), bfhi(r.y), bflo(r.z), bfhi(r.z), bflo(r.w), bfhi(r.w)};
;     float ss = 0.f;
; #pragma unroll
;     for (int e = 0; e < 8; ++e) ss += x[e] * x[e];
;     ss += dpp_x1(ss); ss += dpp_x2(ss); ss += dpp_hm(ss);
;     const float rstd = rsqrtf(ss * (1.f / 64.f) + NORM_EPS);
;     float o[8];
; #pragma unroll
;     for (int e = 0; e < 8; ++e) { const float y = x[e] * rstd * w[e]; o[e] = y * cs[e] + dpp_x2(y) * sn[e]; }
;     u32x4 q; q.x = pk2(o[0], o[1]); q.y = pk2(o[2], o[3]); q.z = pk2(o[4], o[5]); q.w = pk2(o[6], o[7]);
;     *(u32x4*)p = q;
; }
; __device__ __forceinline__ void prep_qk_rows4(KP Pk, Frame& F, int l, int row0) {
;     ...
;     for (int r = 0; r < 4; ++r) { bf16_t* up = U + (size_t)(row0 + r) * NU + 8 * F.lane;
;         qk_vec(up + UC_SQ, raw[r][0], wsq, cs[r], sn[r]); qk_vec(up + UC_DQ, raw[r][1], wdq, cs[r], sn[r]); qk_vec(up + UC_DK, raw[r][2], wdk, cs[r], sn[r]); }
	v_lshlrev_b32_e32 v107, 16, v97
	v_and_b32_e32 v97, 0xffff0000, v97
	v_pk_mul_f32 v[108:109], v[108:109], v[108:109]
	v_pk_mul_f32 v[92:93], v[92:93], v[92:93]
	v_pk_add_f32 v[90:91], v[104:105], v[90:91]
	v_mov_b32_e32 v103, v228
	v_mov_b32_e32 v114, v97
	v_mov_b32_e32 v115, v107
	v_mov_b32_e32 v251, v243
	v_pk_add_f32 v[90:91], v[102:103], v[90:91]
	v_mov_b32_e32 v102, v93
	v_mov_b32_e32 v103, v109
	v_pk_mul_f32 v[114:115], v[114:115], v[114:115]
	v_pk_mul_f32 v[250:251], v[250:251], v[250:251]
	v_pk_add_f32 v[90:91], v[102:103], v[90:91]
	v_mov_b32_e32 v93, v108
	v_pk_add_f32 v[90:91], v[92:93], v[90:91]
	v_mov_b32_e32 v92, v251
	v_mov_b32_e32 v93, v115
	v_pk_add_f32 v[90:91], v[92:93], v[90:91]
	v_mov_b32_e32 v251, v114
	v_pk_add_f32 v[90:91], v[250:251], v[90:91]
	v_mov_b32_e32 v189, v85
	v_mov_b32_e32 v191, v81
	v_mov_b32_dpp v93, v91 quad_perm:[1,0,3,2] row_mask:0xf bank_mask:0xf bound_ctrl:1
	v_mov_b32_dpp v92, v90 quad_perm:[1,0,3,2] row_mask:0xf bank_mask:0xf bound_ctrl:1
	v_pk_add_f32 v[90:91], v[90:91], v[92:93]
	v_mov_b32_e32 v177, v73
	v_lshl_add_u64 v[218:219], v[162:163], 0, s[18:19]
	v_mov_b32_dpp v93, v91 quad_perm:[2,3,0,1] row_mask:0xf bank_mask:0xf bound_ctrl:1
	v_mov_b32_dpp v92, v90 quad_perm:[2,3,0,1] row_mask:0xf bank_mask:0xf bound_ctrl:1
	v_pk_add_f32 v[90:91], v[90:91], v[92:93]
	v_lshl_add_u64 v[192:193], v[134:135], 0, s[18:19]
	v_lshl_add_u64 v[164:165], v[132:133], 0, s[18:19]
	v_mov_b32_dpp v93, v91 row_half_mirror row_mask:0xf bank_mask:0xf bound_ctrl:1
	v_mov_b32_dpp v92, v90 row_half_mirror row_mask:0xf bank_mask:0xf bound_ctrl:1
	v_pk_add_f32 v[90:91], v[90:91], v[92:93]
	v_mov_b64_e32 v[92:93], s[8:9]
	s_mov_b32 s8, 0x3c800000
	v_pk_fma_f32 v[102:103], v[90:91], s[8:9], v[92:93] op_sel_hi:[1,0,0]
	v_mov_b32_e32 v90, v34
	v_mul_f32_e32 v67, 0x4b800000, v103
	v_cmp_gt_f32_e32 vcc, s66, v103
	v_mov_b32_e32 v91, v36
	v_mov_b32_e32 v36, v35
	v_cndmask_b32_e32 v67, v103, v67, vcc
	v_rsq_f32_e32 v67, v67
	s_nop 0
	v_mul_f32_e32 v34, 0x45800000, v67
	v_cndmask_b32_e32 v34, v67, v34, vcc
	v_pk_mul_f32 v[100:101], v[34:35], v[100:101] op_sel_hi:[0,1]
	v_pk_mul_f32 v[100:101], v[20:21], v[100:101]
	v_pk_mul_f32 v[94:95], v[34:35], v[94:95] op_sel_hi:[0,1]
	v_pk_mul_f32 v[94:95], v[16:17], v[94:95]
	v_mov_b32_dpp v104, v100 quad_perm:[2,3,0,1] row_mask:0xf bank_mask:0xf bound_ctrl:1
	v_pk_mul_f32 v[114:115], v[214:215], v[100:101]
	v_mov_b32_dpp v105, v101 quad_perm:[2,3,0,1] row_mask:0xf bank_mask:0xf bound_ctrl:1
	v_mov_b32_dpp v108, v94 quad_perm:[2,3,0,1] row_mask:0xf bank_mask:0xf bound_ctrl:1
	v_pk_fma_f32 v[100:101], v[206:207], v[104:105], v[114:115]
	v_pk_mul_f32 v[104:105], v[212:213], v[94:95]
	v_mov_b32_dpp v109, v95 quad_perm:[2,3,0,1] row_mask:0xf bank_mask:0xf bound_ctrl:1
	v_pk_fma_f32 v[94:95], v[202:203], v[108:109], v[104:105]
	v_pk_mul_f32 v[104:105], v[34:35], v[106:107] op_sel_hi:[0,1]
	v_pk_mul_f32 v[104:105], v[12:13], v[104:105]
	v_pk_mul_f32 v[34:35], v[34:35], v[96:97] op_sel_hi:[0,1]
	v_pk_mul_f32 v[34:35], v[8:9], v[34:35]
	v_mov_b32_dpp v106, v104 quad_perm:[2,3,0,1] row_mask:0xf bank_mask:0xf bound_ctrl:1
	v_pk_mul_f32 v[108:109], v[210:211], v[104:105]
	v_mov_b32_dpp v107, v105 quad_perm:[2,3,0,1] row_mask:0xf bank_mask:0xf bound_ctrl:1
	v_mov_b32_dpp v96, v34 quad_perm:[2,3,0,1] row_mask:0xf bank_mask:0xf bound_ctrl:1
	v_pk_fma_f32 v[104:105], v[200:201], v[106:107], v[108:109]
	v_pk_mul_f32 v[106:107], v[208:209], v[34:35]
	v_mov_b32_dpp v97, v35 quad_perm:[2,3,0,1] row_mask:0xf bank_mask:0xf bound_ctrl:1
	v_pk_fma_f32 v[34:35], v[204:205], v[96:97], v[106:107]
	v_cvt_pk_bf16_f32 v96, v104, v34
	v_mul_f32_e32 v34, 0x4b800000, v102
	v_cmp_gt_f32_e32 vcc, s66, v102
	v_bfe_u32 v67, v35, 16, 1
	v_bfe_u32 v79, v94, 16, 1
	v_cndmask_b32_e32 v34, v102, v34, vcc
	v_rsq_f32_e32 v34, v34
	v_add3_u32 v79, v94, v79, s23
	v_add3_u32 v35, v35, v67, s23
	v_cvt_pk_bf16_f32 v67, v100, 0
	v_cvt_pk_bf16_f32 v94, v105, 0
	v_and_or_b32 v97, v35, s95, v94
	v_cvt_pk_bf16_f32 v95, v101, v95
	v_and_or_b32 v94, v79, s95, v67
	v_mul_f32_e32 v35, 0x45800000, v34
	global_store_dwordx4 v[224:225], v[94:97], off
	v_and_b32_e32 v108, 0xffff0000, v74
	v_and_b32_e32 v109, 0xffff0000, v75
	v_cndmask_b32_e32 v94, v34, v35, vcc
	v_pk_mul_f32 v[34:35], v[94:95], v[116:117] op_sel_hi:[0,1]
	v_pk_mul_f32 v[100:101], v[94:95], v[198:199] op_sel_hi:[0,1]
	v_pk_mul_f32 v[34:35], v[90:91], v[34:35]
	v_pk_mul_f32 v[100:101], v[36:37], v[100:101]
	v_pk_mul_f32 v[104:105], v[214:215], v[34:35]
	v_mov_b32_dpp v96, v34 quad_perm:[2,3,0,1] row_mask:0xf bank_mask:0xf bound_ctrl:1
	v_mov_b32_dpp v102, v100 quad_perm:[2,3,0,1] row_mask:0xf bank_mask:0xf bound_ctrl:1
	v_mov_b32_dpp v97, v35 quad_perm:[2,3,0,1] row_mask:0xf bank_mask:0xf bound_ctrl:1
	v_pk_mul_f32 v[34:35], v[212:213], v[100:101]
	v_mov_b32_dpp v103, v101 quad_perm:[2,3,0,1] row_mask:0xf bank_mask:0xf bound_ctrl:1
	v_pk_fma_f32 v[100:101], v[202:203], v[102:103], v[34:35]
	v_pk_mul_f32 v[102:103], v[94:95], v[242:243] op_sel_hi:[0,1]
	v_mov_b32_e32 v34, v26
	v_mov_b32_e32 v35, v28
	v_pk_mul_f32 v[94:95], v[94:95], v[244:245] op_sel_hi:[0,1]
	v_mov_b32_e32 v28, v27
	v_pk_mul_f32 v[102:103], v[34:35], v[102:103]
	v_pk_mul_f32 v[94:95], v[28:29], v[94:95]
	v_pk_fma_f32 v[96:97], v[206:207], v[96:97], v[104:105]
	v_mov_b32_dpp v26, v102 quad_perm:[2,3,0,1] row_mask:0xf bank_mask:0xf bound_ctrl:1
	v_mov_b32_dpp v104, v94 quad_perm:[2,3,0,1] row_mask:0xf bank_mask:0xf bound_ctrl:1
	v_pk_mul_f32 v[106:107], v[210:211], v[102:103]
	v_mov_b32_dpp v27, v103 quad_perm:[2,3,0,1] row_mask:0xf bank_mask:0xf bound_ctrl:1
	v_pk_mul_f32 v[102:103], v[208:209], v[94:95]
; __device__ __forceinline__ unsigned pk2(float lo, float hi) { return f2bf(lo) | (f2bf(hi) << 16); }
; __device__ __forceinline__ float dpp_x1(float v) { return __builtin_bit_cast(float, __builtin_amdgcn_update_dpp(0, __builtin_bit_cast(int, v), 0xB1, 0xF, 0xF, true)); }
; __device__ __forceinline__ float dpp_x2(float v) { return __builtin_bit_cast(float, __builtin_amdgcn_update_dpp(0, __builtin_bit_cast(int, v), 0x4E, 0xF, 0xF, true)); }
; __device__ __forceinline__ float dpp_hm(float v) { return __builtin_bit_cast(float, __builtin_amdgcn_update_dpp(0, __builtin_bit_cast(int, v), 0x141, 0xF, 0xF, true)); }
; __device__ __forceinline__ void qk_vec(bf16_t* p, const u32x4 r, const float (&w)[8], const float (&cs)[8], const float (&sn)[8]) {
;     float x[8] = {bflo(r.x), bfhi(r.x), bflo(r.y), bfhi(r.y), bflo(r.z), bfhi(r.z), bflo(r.w), bfhi(r.w)};
;     float ss = 0.f;
; #pragma unroll
;     for (int e = 0; e < 8; ++e) ss += x[e] * x[e];
;     ss += dpp_x1(ss); ss += dpp_x2(ss); ss += dpp_hm(ss);
;     const float rstd = rsqrtf(ss * (1.f / 64.f) + NORM_EPS);
;     float o[8];
; #pragma unroll
;     for (int e = 0; e < 8; ++e) { const float y = x[e] * rstd * w[e]; o[e] = y * cs[e] + dpp_x2(y) * sn[e]; }
;     u32x4 q; q.x = pk2(o[0], o[1]); q.y = pk2(o[2], o[3]); q.z = pk2(o[4], o[5]); q.w = pk2(o[6], o[7]);
;     *(u32x4*)p = q;
; }
; __device__ __forceinline__ void prep_qk_rows4(KP Pk, Frame& F, int l, int row0) {
;     ...
;     for (int r = 0; r < 4; ++r) { bf16_t* up = U + (size_t)(row0 + r) * NU + 8 * F.lane;
;         qk_vec(up + UC_SQ, raw[r][0], wsq, cs[r], sn[r]); qk_vec(up + UC_DQ, raw[r][1], wdq, cs[r], sn[r]); qk_vec(up + UC_DK, raw[r][2], wdk, cs[r], sn[r]); }
;     qk_vec(U + (size_t)rowk * NU + UC_SK + 8 * (F.lane & 15), rawk, wsk, csk, snk);
	v_mov_b32_dpp v105, v95 quad_perm:[2,3,0,1] row_mask:0xf bank_mask:0xf bound_ctrl:1
	v_pk_fma_f32 v[94:95], v[204:205], v[104:105], v[102:103]
	v_pk_fma_f32 v[26:27], v[200:201], v[26:27], v[106:107]
	v_bfe_u32 v67, v95, 16, 1
	v_bfe_u32 v69, v94, 16, 1
	v_bfe_u32 v79, v100, 16, 1
	v_add3_u32 v79, v100, v79, s23
	v_add3_u32 v69, v94, v69, s23
	v_add3_u32 v67, v95, v67, s23
	v_bfe_u32 v71, v101, 16, 1
	v_add3_u32 v71, v101, v71, s23
	v_cvt_pk_bf16_f32 v83, v96, 0
	v_cvt_pk_bf16_f32 v94, v97, 0
	v_cvt_pk_bf16_f32 v26, v26, 0
	v_cvt_pk_bf16_f32 v27, v27, 0
	v_and_or_b32 v97, v67, s95, v27
	v_and_or_b32 v96, v69, s95, v26
	v_and_or_b32 v95, v71, s95, v94
	v_and_or_b32 v94, v79, s95, v83
	v_lshlrev_b32_e32 v26, 16, v86
	v_and_b32_e32 v86, 0xffff0000, v86
	v_lshlrev_b32_e32 v106, 16, v74
	global_store_dwordx4 v[222:223], v[94:97], off
	v_lshlrev_b32_e32 v107, 16, v75
	v_mov_b32_e32 v74, v106
	v_mov_b32_e32 v94, v26
	v_mov_b32_e32 v95, v86
	v_mov_b32_e32 v75, v108
	v_pk_mul_f32 v[94:95], v[94:95], v[94:95]
	v_pk_mul_f32 v[74:75], v[74:75], v[74:75]
	v_lshlrev_b32_e32 v27, 16, v87
	v_and_b32_e32 v87, 0xffff0000, v87
	v_mov_b32_e32 v114, v74
	v_mov_b32_e32 v115, v94
	v_mov_b32_e32 v94, v75
	v_mov_b32_e32 v96, v87
	v_mov_b32_e32 v97, v27
	v_pk_add_f32 v[74:75], v[114:115], v[94:95]
	v_mov_b32_e32 v94, v109
	v_mov_b32_e32 v95, v107
	v_pk_mul_f32 v[96:97], v[96:97], v[96:97]
	v_lshlrev_b32_e32 v100, 16, v88
	v_and_b32_e32 v88, 0xffff0000, v88
	v_pk_mul_f32 v[94:95], v[94:95], v[94:95]
	v_lshlrev_b32_e32 v114, 16, v76
	v_and_b32_e32 v116, 0xffff0000, v76
	v_mov_b32_e32 v102, v88
	v_mov_b32_e32 v103, v100
	v_lshlrev_b32_e32 v115, 16, v77
	v_and_b32_e32 v117, 0xffff0000, v77
	v_mov_b32_e32 v76, v116
	v_mov_b32_e32 v77, v114
	v_mov_b32_e32 v200, v95
	v_mov_b32_e32 v201, v97
	v_lshlrev_b32_e32 v101, 16, v89
	v_and_b32_e32 v89, 0xffff0000, v89
	v_pk_mul_f32 v[102:103], v[102:103], v[102:103]
	v_pk_mul_f32 v[76:77], v[76:77], v[76:77]
	v_pk_add_f32 v[74:75], v[200:201], v[74:75]
	v_mov_b32_e32 v95, v96
	v_mov_b32_e32 v104, v89
	v_mov_b32_e32 v105, v101
	v_mov_b32_e32 v198, v117
	v_mov_b32_e32 v199, v115
	v_pk_add_f32 v[74:75], v[94:95], v[74:75]
	v_mov_b32_e32 v94, v77
	v_mov_b32_e32 v95, v103
	v_pk_mul_f32 v[104:105], v[104:105], v[104:105]
	v_pk_mul_f32 v[198:199], v[198:199], v[198:199]
	v_pk_add_f32 v[74:75], v[94:95], v[74:75]
	v_mov_b32_e32 v77, v102
	v_pk_add_f32 v[74:75], v[76:77], v[74:75]
	v_mov_b32_e32 v76, v199
	v_mov_b32_e32 v77, v105
	v_pk_add_f32 v[74:75], v[76:77], v[74:75]
	v_mov_b32_e32 v199, v104
	v_pk_add_f32 v[74:75], v[198:199], v[74:75]
	v_mov_b32_e32 v83, v84
	v_mov_b32_e32 v79, v80
	v_mov_b32_dpp v77, v75 quad_perm:[1,0,3,2] row_mask:0xf bank_mask:0xf bound_ctrl:1
	v_mov_b32_dpp v76, v74 quad_perm:[1,0,3,2] row_mask:0xf bank_mask:0xf bound_ctrl:1
	v_pk_add_f32 v[74:75], v[74:75], v[76:77]
	v_lshlrev_b32_e32 v96, 16, v58
	v_lshlrev_b32_e32 v97, 16, v59
	v_mov_b32_dpp v77, v75 quad_perm:[2,3,0,1] row_mask:0xf bank_mask:0xf bound_ctrl:1
	v_mov_b32_dpp v76, v74 quad_perm:[2,3,0,1] row_mask:0xf bank_mask:0xf bound_ctrl:1
	v_pk_add_f32 v[74:75], v[74:75], v[76:77]
	v_and_b32_e32 v104, 0xffff0000, v60
	v_and_b32_e32 v105, 0xffff0000, v61
	v_mov_b32_dpp v77, v75 row_half_mirror row_mask:0xf bank_mask:0xf bound_ctrl:1
	v_mov_b32_dpp v76, v74 row_half_mirror row_mask:0xf bank_mask:0xf bound_ctrl:1
	v_pk_add_f32 v[74:75], v[74:75], v[76:77]
	s_nop 0
	v_pk_fma_f32 v[74:75], v[74:75], s[8:9], v[92:93] op_sel_hi:[1,0,0]
	s_nop 0
	v_mul_f32_e32 v67, 0x4b800000, v75
	v_cmp_gt_f32_e32 vcc, s66, v75
	s_nop 1
	v_cndmask_b32_e32 v67, v75, v67, vcc
	v_rsq_f32_e32 v67, v67
	s_nop 0
	v_mul_f32_e32 v69, 0x45800000, v67
	v_cndmask_b32_e32 v76, v67, v69, vcc
	v_pk_mul_f32 v[26:27], v[76:77], v[26:27] op_sel_hi:[0,1]
	v_pk_mul_f32 v[26:27], v[98:99], v[26:27]
	v_pk_mul_f32 v[84:85], v[76:77], v[86:87] op_sel_hi:[0,1]
	v_pk_mul_f32 v[84:85], v[112:113], v[84:85]
	v_mov_b32_dpp v80, v26 quad_perm:[2,3,0,1] row_mask:0xf bank_mask:0xf bound_ctrl:1
	v_pk_mul_f32 v[94:95], v[82:83], v[26:27]
	v_mov_b32_dpp v81, v27 quad_perm:[2,3,0,1] row_mask:0xf bank_mask:0xf bound_ctrl:1
	v_mov_b32_dpp v86, v84 quad_perm:[2,3,0,1] row_mask:0xf bank_mask:0xf bound_ctrl:1
	v_pk_fma_f32 v[26:27], v[184:185], v[80:81], v[94:95]
	v_pk_mul_f32 v[80:81], v[188:189], v[84:85]
	v_mov_b32_dpp v87, v85 quad_perm:[2,3,0,1] row_mask:0xf bank_mask:0xf bound_ctrl:1
	v_pk_mul_f32 v[84:85], v[76:77], v[100:101] op_sel_hi:[0,1]
	v_pk_mul_f32 v[84:85], v[110:111], v[84:85]
	v_pk_mul_f32 v[76:77], v[76:77], v[88:89] op_sel_hi:[0,1]
	v_pk_fma_f32 v[80:81], v[182:183], v[86:87], v[80:81]
	v_mov_b32_dpp v86, v84 quad_perm:[2,3,0,1] row_mask:0xf bank_mask:0xf bound_ctrl:1
	v_pk_mul_f32 v[76:77], v[196:197], v[76:77]
	v_pk_mul_f32 v[94:95], v[78:79], v[84:85]
	v_mov_b32_dpp v87, v85 quad_perm:[2,3,0,1] row_mask:0xf bank_mask:0xf bound_ctrl:1
	v_mov_b32_dpp v88, v76 quad_perm:[2,3,0,1] row_mask:0xf bank_mask:0xf bound_ctrl:1
	v_pk_fma_f32 v[84:85], v[180:181], v[86:87], v[94:95]
	v_pk_mul_f32 v[86:87], v[190:191], v[76:77]
	v_mov_b32_dpp v89, v77 quad_perm:[2,3,0,1] row_mask:0xf bank_mask:0xf bound_ctrl:1
	v_pk_fma_f32 v[76:77], v[186:187], v[88:89], v[86:87]
	v_bfe_u32 v71, v81, 16, 1
	v_bfe_u32 v67, v77, 16, 1
	v_bfe_u32 v69, v76, 16, 1
	v_add3_u32 v71, v81, v71, s23
	v_bfe_u32 v75, v80, 16, 1
	v_add3_u32 v69, v76, v69, s23
	v_add3_u32 v67, v77, v67, s23
	v_bfe_u32 v76, v27, 16, 1
	v_add3_u32 v80, v80, v75, s23
	v_bfe_u32 v75, v26, 16, 1
	v_add3_u32 v27, v27, v76, s23
	v_cvt_pk_bf16_f32 v76, v85, 0
	v_add3_u32 v26, v26, v75, s23
	v_cvt_pk_bf16_f32 v75, v84, 0
	v_and_or_b32 v77, v67, s95, v76
; __device__ __forceinline__ unsigned pk2(float lo, float hi) { return f2bf(lo) | (f2bf(hi) << 16); }
; __device__ __forceinline__ float dpp_x1(float v) { return __builtin_bit_cast(float, __builtin_amdgcn_update_dpp(0, __builtin_bit_cast(int, v), 0xB1, 0xF, 0xF, true)); }
; __device__ __forceinline__ float dpp_x2(float v) { return __builtin_bit_cast(float, __builtin_amdgcn_update_dpp(0, __builtin_bit_cast(int, v), 0x4E, 0xF, 0xF, true)); }
; __device__ __forceinline__ float dpp_hm(float v) { return __builtin_bit_cast(float, __builtin_amdgcn_update_dpp(0, __builtin_bit_cast(int, v), 0x141, 0xF, 0xF, true)); }
; __device__ __forceinline__ void qk_vec(bf16_t* p, const u32x4 r, const float (&w)[8], const float (&cs)[8], const float (&sn)[8]) {
;     float x[8] = {bflo(r.x), bfhi(r.x), bflo(r.y), bfhi(r.y), bflo(r.z), bfhi(r.z), bflo(r.w), bfhi(r.w)};
;     float ss = 0.f;
; #pragma unroll
;     for (int e = 0; e < 8; ++e) ss += x[e] * x[e];
;     ss += dpp_x1(ss); ss += dpp_x2(ss); ss += dpp_hm(ss);
;     const float rstd = rsqrtf(ss * (1.f / 64.f) + NORM_EPS);
;     float o[8];
; #pragma unroll
;     for (int e = 0; e < 8; ++e) { const float y = x[e] * rstd * w[e]; o[e] = y * cs[e] + dpp_x2(y) * sn[e]; }
;     u32x4 q; q.x = pk2(o[0], o[1]); q.y = pk2(o[2], o[3]); q.z = pk2(o[4], o[5]); q.w = pk2(o[6], o[7]);
;     *(u32x4*)p = q;
; }
; __device__ __forceinline__ void prep_qk_rows4(KP Pk, Frame& F, int l, int row0) {
;     ...
;     for (int r = 0; r < 4; ++r) { bf16_t* up = U + (size_t)(row0 + r) * NU + 8 * F.lane;
;         qk_vec(up + UC_SQ, raw[r][0], wsq, cs[r], sn[r]); qk_vec(up + UC_DQ, raw[r][1], wdq, cs[r], sn[r]); qk_vec(up + UC_DK, raw[r][2], wdk, cs[r], sn[r]); }
;     qk_vec(U + (size_t)rowk * NU + UC_SK + 8 * (F.lane & 15), rawk, wsk, csk, snk);
	v_mul_f32_e32 v67, 0x4b800000, v74
	v_cmp_gt_f32_e32 vcc, s66, v74
	v_lshrrev_b32_e32 v26, 16, v26
	v_lshrrev_b32_e32 v27, 16, v27
	v_cndmask_b32_e32 v67, v74, v67, vcc
	v_rsq_f32_e32 v67, v67
	v_and_or_b32 v74, v80, s95, v26
	v_and_or_b32 v76, v69, s95, v75
	v_and_or_b32 v75, v71, s95, v27
	v_mul_f32_e32 v26, 0x45800000, v67
	v_cndmask_b32_e32 v26, v67, v26, vcc
	global_store_dwordx4 v[162:163], v[74:77], off offset:3072
	v_pk_mul_f32 v[80:81], v[26:27], v[108:109] op_sel_hi:[0,1]
	v_pk_mul_f32 v[80:81], v[16:17], v[80:81]
	v_pk_mul_f32 v[74:75], v[26:27], v[106:107] op_sel_hi:[0,1]
	v_pk_mul_f32 v[74:75], v[20:21], v[74:75]
	v_mov_b32_dpp v84, v80 quad_perm:[2,3,0,1] row_mask:0xf bank_mask:0xf bound_ctrl:1
	v_pk_mul_f32 v[86:87], v[82:83], v[74:75]
	v_mov_b32_dpp v76, v74 quad_perm:[2,3,0,1] row_mask:0xf bank_mask:0xf bound_ctrl:1
	v_mov_b32_dpp v77, v75 quad_perm:[2,3,0,1] row_mask:0xf bank_mask:0xf bound_ctrl:1
	v_pk_fma_f32 v[74:75], v[184:185], v[76:77], v[86:87]
	v_pk_mul_f32 v[76:77], v[188:189], v[80:81]
	v_mov_b32_dpp v85, v81 quad_perm:[2,3,0,1] row_mask:0xf bank_mask:0xf bound_ctrl:1
	v_pk_mul_f32 v[80:81], v[26:27], v[114:115] op_sel_hi:[0,1]
	v_pk_mul_f32 v[80:81], v[12:13], v[80:81]
	v_pk_mul_f32 v[26:27], v[26:27], v[116:117] op_sel_hi:[0,1]
	v_pk_fma_f32 v[76:77], v[182:183], v[84:85], v[76:77]
	v_mov_b32_dpp v84, v80 quad_perm:[2,3,0,1] row_mask:0xf bank_mask:0xf bound_ctrl:1
	v_pk_mul_f32 v[26:27], v[8:9], v[26:27]
	v_pk_mul_f32 v[88:89], v[78:79], v[80:81]
	v_mov_b32_dpp v85, v81 quad_perm:[2,3,0,1] row_mask:0xf bank_mask:0xf bound_ctrl:1
	v_mov_b32_dpp v86, v26 quad_perm:[2,3,0,1] row_mask:0xf bank_mask:0xf bound_ctrl:1
	v_pk_fma_f32 v[80:81], v[180:181], v[84:85], v[88:89]
	v_pk_mul_f32 v[84:85], v[190:191], v[26:27]
	v_mov_b32_dpp v87, v27 quad_perm:[2,3,0,1] row_mask:0xf bank_mask:0xf bound_ctrl:1
	v_pk_fma_f32 v[26:27], v[186:187], v[86:87], v[84:85]
	v_bfe_u32 v84, v76, 16, 1
	v_bfe_u32 v67, v27, 16, 1
	v_add3_u32 v84, v76, v84, s23
	v_add3_u32 v27, v27, v67, s23
	v_bfe_u32 v71, v77, 16, 1
	v_add3_u32 v71, v77, v71, s23
	v_bfe_u32 v77, v81, 16, 1
	v_cvt_pk_bf16_f32 v76, v80, v26
	v_lshlrev_b32_e32 v26, 16, v62
	v_and_b32_e32 v62, 0xffff0000, v62
	v_and_b32_e32 v100, 0xffff0000, v58
	v_bfe_u32 v69, v75, 16, 1
	v_add3_u32 v77, v81, v77, s23
	v_mov_b32_e32 v80, v26
	v_mov_b32_e32 v81, v62
	v_and_b32_e32 v101, 0xffff0000, v59
	v_mov_b32_e32 v58, v96
	v_mov_b32_e32 v59, v100
	v_add3_u32 v69, v75, v69, s23
	v_lshrrev_b32_e32 v75, 16, v77
	v_pk_mul_f32 v[80:81], v[80:81], v[80:81]
	v_pk_mul_f32 v[58:59], v[58:59], v[58:59]
	v_cvt_pk_bf16_f32 v67, v74, 0
	v_and_or_b32 v77, v27, s95, v75
	v_lshlrev_b32_e32 v27, 16, v63
	v_and_b32_e32 v63, 0xffff0000, v63
	v_mov_b32_e32 v102, v58
	v_mov_b32_e32 v103, v80
	v_mov_b32_e32 v80, v59
	v_and_or_b32 v74, v84, s95, v67
	v_mov_b32_e32 v84, v63
	v_mov_b32_e32 v85, v27
	v_pk_add_f32 v[58:59], v[102:103], v[80:81]
	v_mov_b32_e32 v80, v101
	v_mov_b32_e32 v81, v97
	v_pk_mul_f32 v[84:85], v[84:85], v[84:85]
	v_lshlrev_b32_e32 v86, 16, v64
	v_and_b32_e32 v64, 0xffff0000, v64
	v_pk_mul_f32 v[80:81], v[80:81], v[80:81]
	v_lshlrev_b32_e32 v102, 16, v60
	v_mov_b32_e32 v88, v64
	v_mov_b32_e32 v89, v86
	v_lshlrev_b32_e32 v103, 16, v61
	v_mov_b32_e32 v60, v104
	v_mov_b32_e32 v61, v102
	v_mov_b32_e32 v108, v81
	v_mov_b32_e32 v109, v85
	v_lshlrev_b32_e32 v87, 16, v65
	v_and_b32_e32 v65, 0xffff0000, v65
	v_pk_mul_f32 v[88:89], v[88:89], v[88:89]
	v_pk_mul_f32 v[60:61], v[60:61], v[60:61]
	v_pk_add_f32 v[58:59], v[108:109], v[58:59]
	v_mov_b32_e32 v81, v84
	v_mov_b32_e32 v94, v65
	v_mov_b32_e32 v95, v87
	v_mov_b32_e32 v106, v105
	v_mov_b32_e32 v107, v103
	v_pk_add_f32 v[58:59], v[80:81], v[58:59]
	v_mov_b32_e32 v80, v61
	v_mov_b32_e32 v81, v89
	v_pk_mul_f32 v[94:95], v[94:95], v[94:95]
	v_pk_mul_f32 v[106:107], v[106:107], v[106:107]
	v_pk_add_f32 v[58:59], v[80:81], v[58:59]
	v_mov_b32_e32 v61, v88
	v_pk_add_f32 v[58:59], v[60:61], v[58:59]
	v_mov_b32_e32 v60, v107
	v_mov_b32_e32 v61, v95
	v_pk_add_f32 v[58:59], v[60:61], v[58:59]
	v_mov_b32_e32 v107, v94
	v_pk_add_f32 v[58:59], v[106:107], v[58:59]
	v_lshrrev_b32_e32 v69, 16, v69
	v_and_or_b32 v75, v71, s95, v69
	v_mov_b32_dpp v61, v59 quad_perm:[1,0,3,2] row_mask:0xf bank_mask:0xf bound_ctrl:1
	v_mov_b32_dpp v60, v58 quad_perm:[1,0,3,2] row_mask:0xf bank_mask:0xf bound_ctrl:1
	v_pk_add_f32 v[58:59], v[58:59], v[60:61]
	global_store_dwordx4 v[220:221], v[74:77], off
	v_mov_b32_e32 v71, v72
	v_mov_b32_dpp v61, v59 quad_perm:[2,3,0,1] row_mask:0xf bank_mask:0xf bound_ctrl:1
	v_mov_b32_dpp v60, v58 quad_perm:[2,3,0,1] row_mask:0xf bank_mask:0xf bound_ctrl:1
	v_pk_add_f32 v[58:59], v[58:59], v[60:61]
	v_and_b32_e32 v80, 0xffff0000, v52
	v_and_b32_e32 v81, 0xffff0000, v53
	v_mov_b32_dpp v61, v59 row_half_mirror row_mask:0xf bank_mask:0xf bound_ctrl:1
	v_mov_b32_dpp v60, v58 row_half_mirror row_mask:0xf bank_mask:0xf bound_ctrl:1
	v_pk_add_f32 v[58:59], v[58:59], v[60:61]
	s_nop 0
	v_pk_fma_f32 v[58:59], v[58:59], s[8:9], v[92:93] op_sel_hi:[1,0,0]
	s_nop 0
	v_mul_f32_e32 v60, 0x4b800000, v59
	v_cmp_gt_f32_e32 vcc, s66, v59
	s_nop 1
	v_cndmask_b32_e32 v59, v59, v60, vcc
	v_rsq_f32_e32 v59, v59
	s_nop 0
	v_mul_f32_e32 v60, 0x45800000, v59
	v_cndmask_b32_e32 v60, v59, v60, vcc
	v_pk_mul_f32 v[26:27], v[60:61], v[26:27] op_sel_hi:[0,1]
	v_pk_mul_f32 v[26:27], v[90:91], v[26:27]
	v_pk_mul_f32 v[62:63], v[60:61], v[62:63] op_sel_hi:[0,1]
	v_pk_mul_f32 v[62:63], v[36:37], v[62:63]
	v_mov_b32_dpp v72, v26 quad_perm:[2,3,0,1] row_mask:0xf bank_mask:0xf bound_ctrl:1
	v_pk_mul_f32 v[76:77], v[82:83], v[26:27]
	v_mov_b32_dpp v73, v27 quad_perm:[2,3,0,1] row_mask:0xf bank_mask:0xf bound_ctrl:1
; __device__ __forceinline__ unsigned pk2(float lo, float hi) { return f2bf(lo) | (f2bf(hi) << 16); }
; __device__ __forceinline__ float dpp_x1(float v) { return __builtin_bit_cast(float, __builtin_amdgcn_update_dpp(0, __builtin_bit_cast(int, v), 0xB1, 0xF, 0xF, true)); }
; __device__ __forceinline__ float dpp_x2(float v) { return __builtin_bit_cast(float, __builtin_amdgcn_update_dpp(0, __builtin_bit_cast(int, v), 0x4E, 0xF, 0xF, true)); }
; __device__ __forceinline__ float dpp_hm(float v) { return __builtin_bit_cast(float, __builtin_amdgcn_update_dpp(0, __builtin_bit_cast(int, v), 0x141, 0xF, 0xF, true)); }
; __device__ __forceinline__ void qk_vec(bf16_t* p, const u32x4 r, const float (&w)[8], const float (&cs)[8], const float (&sn)[8]) {
;     float x[8] = {bflo(r.x), bfhi(r.x), bflo(r.y), bfhi(r.y), bflo(r.z), bfhi(r.z), bflo(r.w), bfhi(r.w)};
;     float ss = 0.f;
; #pragma unroll
;     for (int e = 0; e < 8; ++e) ss += x[e] * x[e];
;     ss += dpp_x1(ss); ss += dpp_x2(ss); ss += dpp_hm(ss);
;     const float rstd = rsqrtf(ss * (1.f / 64.f) + NORM_EPS);
;     float o[8];
; #pragma unroll
;     for (int e = 0; e < 8; ++e) { const float y = x[e] * rstd * w[e]; o[e] = y * cs[e] + dpp_x2(y) * sn[e]; }
;     u32x4 q; q.x = pk2(o[0], o[1]); q.y = pk2(o[2], o[3]); q.z = pk2(o[4], o[5]); q.w = pk2(o[6], o[7]);
;     *(u32x4*)p = q;
; }
; __device__ __forceinline__ void prep_qk_rows4(KP Pk, Frame& F, int l, int row0) {
;     ...
;     for (int r = 0; r < 4; ++r) { bf16_t* up = U + (size_t)(row0 + r) * NU + 8 * F.lane;
;         qk_vec(up + UC_SQ, raw[r][0], wsq, cs[r], sn[r]); qk_vec(up + UC_DQ, raw[r][1], wdq, cs[r], sn[r]); qk_vec(up + UC_DK, raw[r][2], wdk, cs[r], sn[r]); }
;     qk_vec(U + (size_t)rowk * NU + UC_SK + 8 * (F.lane & 15), rawk, wsk, csk, snk);
	v_mov_b32_dpp v74, v62 quad_perm:[2,3,0,1] row_mask:0xf bank_mask:0xf bound_ctrl:1
	v_pk_fma_f32 v[26:27], v[184:185], v[72:73], v[76:77]
	v_pk_mul_f32 v[72:73], v[188:189], v[62:63]
	v_mov_b32_dpp v75, v63 quad_perm:[2,3,0,1] row_mask:0xf bank_mask:0xf bound_ctrl:1
	v_pk_fma_f32 v[62:63], v[182:183], v[74:75], v[72:73]
	v_pk_mul_f32 v[72:73], v[60:61], v[86:87] op_sel_hi:[0,1]
	v_pk_mul_f32 v[72:73], v[34:35], v[72:73]
	v_pk_mul_f32 v[60:61], v[60:61], v[64:65] op_sel_hi:[0,1]
	v_pk_mul_f32 v[60:61], v[28:29], v[60:61]
	v_mov_b32_dpp v74, v72 quad_perm:[2,3,0,1] row_mask:0xf bank_mask:0xf bound_ctrl:1
	v_pk_mul_f32 v[76:77], v[78:79], v[72:73]
	v_mov_b32_dpp v75, v73 quad_perm:[2,3,0,1] row_mask:0xf bank_mask:0xf bound_ctrl:1
	v_mov_b32_dpp v64, v60 quad_perm:[2,3,0,1] row_mask:0xf bank_mask:0xf bound_ctrl:1
	v_pk_fma_f32 v[72:73], v[180:181], v[74:75], v[76:77]
	v_pk_mul_f32 v[74:75], v[190:191], v[60:61]
	v_mov_b32_dpp v65, v61 quad_perm:[2,3,0,1] row_mask:0xf bank_mask:0xf bound_ctrl:1
	v_pk_fma_f32 v[60:61], v[186:187], v[64:65], v[74:75]
	v_bfe_u32 v67, v62, 16, 1
	v_bfe_u32 v59, v61, 16, 1
	v_add3_u32 v62, v62, v67, s23
	v_bfe_u32 v65, v63, 16, 1
	v_add3_u32 v59, v61, v59, s23
	v_bfe_u32 v61, v26, 16, 1
	v_bfe_u32 v64, v60, 16, 1
	v_add3_u32 v63, v63, v65, s23
	v_bfe_u32 v65, v72, 16, 1
	v_add3_u32 v26, v26, v61, s23
	v_cvt_pk_bf16_f32 v61, v73, 0
	v_add3_u32 v60, v60, v64, s23
	v_bfe_u32 v64, v27, 16, 1
	v_add3_u32 v65, v72, v65, s23
	v_and_or_b32 v61, v59, s95, v61
	v_mul_f32_e32 v59, 0x4b800000, v58
	v_cmp_gt_f32_e32 vcc, s66, v58
	v_add3_u32 v27, v27, v64, s23
	v_lshrrev_b32_e32 v64, 16, v65
	v_cndmask_b32_e32 v58, v58, v59, vcc
	v_and_or_b32 v60, v60, s95, v64
	v_rsq_f32_e32 v64, v58
	v_lshrrev_b32_e32 v26, 16, v26
	v_lshrrev_b32_e32 v27, 16, v27
	v_and_or_b32 v58, v62, s95, v26
	v_mul_f32_e32 v26, 0x45800000, v64
	v_and_or_b32 v59, v63, s95, v27
	v_cndmask_b32_e32 v26, v64, v26, vcc
	global_store_dwordx4 v[218:219], v[58:61], off
	v_pk_mul_f32 v[62:63], v[26:27], v[100:101] op_sel_hi:[0,1]
	v_pk_mul_f32 v[62:63], v[112:113], v[62:63]
	v_pk_mul_f32 v[58:59], v[26:27], v[96:97] op_sel_hi:[0,1]
	v_pk_mul_f32 v[58:59], v[98:99], v[58:59]
	v_mov_b32_dpp v64, v62 quad_perm:[2,3,0,1] row_mask:0xf bank_mask:0xf bound_ctrl:1
	v_pk_mul_f32 v[72:73], v[70:71], v[58:59]
	v_mov_b32_dpp v60, v58 quad_perm:[2,3,0,1] row_mask:0xf bank_mask:0xf bound_ctrl:1
	v_mov_b32_dpp v61, v59 quad_perm:[2,3,0,1] row_mask:0xf bank_mask:0xf bound_ctrl:1
	v_pk_fma_f32 v[58:59], v[170:171], v[60:61], v[72:73]
	v_pk_mul_f32 v[60:61], v[176:177], v[62:63]
	v_mov_b32_dpp v65, v63 quad_perm:[2,3,0,1] row_mask:0xf bank_mask:0xf bound_ctrl:1
	v_pk_mul_f32 v[62:63], v[26:27], v[102:103] op_sel_hi:[0,1]
	v_pk_mul_f32 v[62:63], v[110:111], v[62:63]
	v_pk_mul_f32 v[26:27], v[26:27], v[104:105] op_sel_hi:[0,1]
	v_mov_b32_e32 v67, v68
	v_pk_fma_f32 v[60:61], v[168:169], v[64:65], v[60:61]
	v_mov_b32_dpp v64, v62 quad_perm:[2,3,0,1] row_mask:0xf bank_mask:0xf bound_ctrl:1
	v_pk_mul_f32 v[26:27], v[196:197], v[26:27]
	v_pk_mul_f32 v[68:69], v[66:67], v[62:63]
	v_mov_b32_dpp v65, v63 quad_perm:[2,3,0,1] row_mask:0xf bank_mask:0xf bound_ctrl:1
	v_mov_b32_dpp v72, v26 quad_perm:[2,3,0,1] row_mask:0xf bank_mask:0xf bound_ctrl:1
	v_pk_fma_f32 v[62:63], v[166:167], v[64:65], v[68:69]
	v_pk_mul_f32 v[64:65], v[174:175], v[26:27]
	v_mov_b32_dpp v73, v27 quad_perm:[2,3,0,1] row_mask:0xf bank_mask:0xf bound_ctrl:1
	v_pk_fma_f32 v[26:27], v[172:173], v[72:73], v[64:65]
	v_bfe_u32 v69, v60, 16, 1
	v_bfe_u32 v64, v27, 16, 1
	v_add3_u32 v86, v60, v69, s23
	v_add3_u32 v27, v27, v64, s23
	v_bfe_u32 v65, v26, 16, 1
	v_bfe_u32 v68, v61, 16, 1
	v_add3_u32 v26, v26, v65, s23
	v_cvt_pk_bf16_f32 v88, v58, 0
	v_cvt_pk_bf16_f32 v58, v62, 0
	v_add3_u32 v87, v61, v68, s23
	v_bfe_u32 v61, v59, 16, 1
	v_and_or_b32 v58, v26, s95, v58
	v_lshlrev_b32_e32 v26, 16, v54
	v_and_b32_e32 v54, 0xffff0000, v54
	v_lshlrev_b32_e32 v74, 16, v50
	v_and_b32_e32 v76, 0xffff0000, v50
	v_add3_u32 v59, v59, v61, s23
	v_mov_b32_e32 v60, v26
	v_mov_b32_e32 v61, v54
	v_lshlrev_b32_e32 v75, 16, v51
	v_and_b32_e32 v77, 0xffff0000, v51
	v_mov_b32_e32 v50, v74
	v_mov_b32_e32 v51, v76
	v_lshrrev_b32_e32 v89, 16, v59
	v_cvt_pk_bf16_f32 v59, v63, 0
	v_pk_mul_f32 v[60:61], v[60:61], v[60:61]
	v_pk_mul_f32 v[50:51], v[50:51], v[50:51]
	v_and_or_b32 v59, v27, s95, v59
	v_lshlrev_b32_e32 v27, 16, v55
	v_and_b32_e32 v55, 0xffff0000, v55
	v_mov_b32_e32 v78, v50
	v_mov_b32_e32 v79, v60
	v_mov_b32_e32 v60, v51
	v_mov_b32_e32 v62, v55
	v_mov_b32_e32 v63, v27
	v_pk_add_f32 v[50:51], v[78:79], v[60:61]
	v_mov_b32_e32 v60, v77
	v_mov_b32_e32 v61, v75
	v_pk_mul_f32 v[62:63], v[62:63], v[62:63]
	v_lshlrev_b32_e32 v64, 16, v56
	v_and_b32_e32 v68, 0xffff0000, v56
	v_pk_mul_f32 v[60:61], v[60:61], v[60:61]
	v_lshlrev_b32_e32 v78, 16, v52
	v_lshlrev_b32_e32 v65, 16, v57
	v_and_b32_e32 v69, 0xffff0000, v57
	v_mov_b32_e32 v56, v68
	v_mov_b32_e32 v57, v64
	v_lshlrev_b32_e32 v79, 16, v53
	v_mov_b32_e32 v52, v80
	v_mov_b32_e32 v53, v78
	v_mov_b32_e32 v84, v61
	v_mov_b32_e32 v85, v63
	v_pk_mul_f32 v[56:57], v[56:57], v[56:57]
	v_pk_mul_f32 v[52:53], v[52:53], v[52:53]
	v_pk_add_f32 v[50:51], v[84:85], v[50:51]
	v_mov_b32_e32 v61, v62
	v_mov_b32_e32 v72, v69
	v_mov_b32_e32 v73, v65
	v_mov_b32_e32 v82, v81
	v_mov_b32_e32 v83, v79
	v_pk_add_f32 v[50:51], v[60:61], v[50:51]
	v_mov_b32_e32 v60, v53
	v_mov_b32_e32 v61, v57
	v_pk_mul_f32 v[72:73], v[72:73], v[72:73]
	v_pk_mul_f32 v[82:83], v[82:83], v[82:83]
	v_pk_add_f32 v[50:51], v[60:61], v[50:51]
	v_mov_b32_e32 v53, v56
	v_pk_add_f32 v[50:51], v[52:53], v[50:51]
	v_mov_b32_e32 v52, v83
	v_mov_b32_e32 v53, v73
; __device__ __forceinline__ unsigned pk2(float lo, float hi) { return f2bf(lo) | (f2bf(hi) << 16); }
; __device__ __forceinline__ float dpp_x1(float v) { return __builtin_bit_cast(float, __builtin_amdgcn_update_dpp(0, __builtin_bit_cast(int, v), 0xB1, 0xF, 0xF, true)); }
; __device__ __forceinline__ float dpp_x2(float v) { return __builtin_bit_cast(float, __builtin_amdgcn_update_dpp(0, __builtin_bit_cast(int, v), 0x4E, 0xF, 0xF, true)); }
; __device__ __forceinline__ float dpp_hm(float v) { return __builtin_bit_cast(float, __builtin_amdgcn_update_dpp(0, __builtin_bit_cast(int, v), 0x141, 0xF, 0xF, true)); }
; __device__ __forceinline__ void qk_vec(bf16_t* p, const u32x4 r, const float (&w)[8], const float (&cs)[8], const float (&sn)[8]) {
;     float x[8] = {bflo(r.x), bfhi(r.x), bflo(r.y), bfhi(r.y), bflo(r.z), bfhi(r.z), bflo(r.w), bfhi(r.w)};
;     float ss = 0.f;
; #pragma unroll
;     for (int e = 0; e < 8; ++e) ss += x[e] * x[e];
;     ss += dpp_x1(ss); ss += dpp_x2(ss); ss += dpp_hm(ss);
;     const float rstd = rsqrtf(ss * (1.f / 64.f) + NORM_EPS);
;     float o[8];
; #pragma unroll
;     for (int e = 0; e < 8; ++e) { const float y = x[e] * rstd * w[e]; o[e] = y * cs[e] + dpp_x2(y) * sn[e]; }
;     u32x4 q; q.x = pk2(o[0], o[1]); q.y = pk2(o[2], o[3]); q.z = pk2(o[4], o[5]); q.w = pk2(o[6], o[7]);
;     *(u32x4*)p = q;
; }
; __device__ __forceinline__ void prep_qk_rows4(KP Pk, Frame& F, int l, int row0) {
;     ...
;     for (int r = 0; r < 4; ++r) { bf16_t* up = U + (size_t)(row0 + r) * NU + 8 * F.lane;
;         qk_vec(up + UC_SQ, raw[r][0], wsq, cs[r], sn[r]); qk_vec(up + UC_DQ, raw[r][1], wdq, cs[r], sn[r]); qk_vec(up + UC_DK, raw[r][2], wdk, cs[r], sn[r]); }
;     qk_vec(U + (size_t)rowk * NU + UC_SK + 8 * (F.lane & 15), rawk, wsk, csk, snk);
	v_pk_add_f32 v[50:51], v[52:53], v[50:51]
	v_mov_b32_e32 v83, v72
	v_pk_add_f32 v[50:51], v[82:83], v[50:51]
	v_and_or_b32 v57, v87, s95, v89
	v_and_or_b32 v56, v86, s95, v88
	v_mov_b32_dpp v53, v51 quad_perm:[1,0,3,2] row_mask:0xf bank_mask:0xf bound_ctrl:1
	v_mov_b32_dpp v52, v50 quad_perm:[1,0,3,2] row_mask:0xf bank_mask:0xf bound_ctrl:1
	v_pk_add_f32 v[50:51], v[50:51], v[52:53]
	global_store_dwordx4 v[134:135], v[56:59], off offset:3072
	s_nop 0
	v_mov_b32_dpp v53, v51 quad_perm:[2,3,0,1] row_mask:0xf bank_mask:0xf bound_ctrl:1
	v_mov_b32_dpp v52, v50 quad_perm:[2,3,0,1] row_mask:0xf bank_mask:0xf bound_ctrl:1
	v_pk_add_f32 v[50:51], v[50:51], v[52:53]
	s_nop 1
	v_mov_b32_dpp v53, v51 row_half_mirror row_mask:0xf bank_mask:0xf bound_ctrl:1
	v_mov_b32_dpp v52, v50 row_half_mirror row_mask:0xf bank_mask:0xf bound_ctrl:1
	v_pk_add_f32 v[50:51], v[50:51], v[52:53]
	s_nop 0
	v_pk_fma_f32 v[50:51], v[50:51], s[8:9], v[92:93] op_sel_hi:[1,0,0]
	s_nop 0
	v_mul_f32_e32 v52, 0x4b800000, v51
	v_cmp_gt_f32_e32 vcc, s66, v51
	s_nop 1
	v_cndmask_b32_e32 v51, v51, v52, vcc
	v_rsq_f32_e32 v51, v51
	s_nop 0
	v_mul_f32_e32 v52, 0x45800000, v51
	v_cndmask_b32_e32 v52, v51, v52, vcc
	v_pk_mul_f32 v[26:27], v[52:53], v[26:27] op_sel_hi:[0,1]
	v_pk_mul_f32 v[26:27], v[20:21], v[26:27]
	v_pk_mul_f32 v[54:55], v[52:53], v[54:55] op_sel_hi:[0,1]
	v_pk_mul_f32 v[54:55], v[16:17], v[54:55]
	v_mov_b32_dpp v56, v26 quad_perm:[2,3,0,1] row_mask:0xf bank_mask:0xf bound_ctrl:1
	v_pk_mul_f32 v[60:61], v[70:71], v[26:27]
	v_mov_b32_dpp v57, v27 quad_perm:[2,3,0,1] row_mask:0xf bank_mask:0xf bound_ctrl:1
	v_mov_b32_dpp v58, v54 quad_perm:[2,3,0,1] row_mask:0xf bank_mask:0xf bound_ctrl:1
	v_pk_fma_f32 v[26:27], v[170:171], v[56:57], v[60:61]
	v_pk_mul_f32 v[56:57], v[176:177], v[54:55]
	v_mov_b32_dpp v59, v55 quad_perm:[2,3,0,1] row_mask:0xf bank_mask:0xf bound_ctrl:1
	v_pk_fma_f32 v[54:55], v[168:169], v[58:59], v[56:57]
	v_pk_mul_f32 v[56:57], v[52:53], v[64:65] op_sel_hi:[0,1]
	v_pk_mul_f32 v[56:57], v[12:13], v[56:57]
	v_pk_mul_f32 v[52:53], v[52:53], v[68:69] op_sel_hi:[0,1]
	v_pk_mul_f32 v[52:53], v[8:9], v[52:53]
	v_mov_b32_dpp v58, v56 quad_perm:[2,3,0,1] row_mask:0xf bank_mask:0xf bound_ctrl:1
	v_pk_mul_f32 v[62:63], v[66:67], v[56:57]
	v_mov_b32_dpp v59, v57 quad_perm:[2,3,0,1] row_mask:0xf bank_mask:0xf bound_ctrl:1
	v_mov_b32_dpp v60, v52 quad_perm:[2,3,0,1] row_mask:0xf bank_mask:0xf bound_ctrl:1
	v_pk_fma_f32 v[56:57], v[166:167], v[58:59], v[62:63]
	v_pk_mul_f32 v[58:59], v[174:175], v[52:53]
	v_mov_b32_dpp v61, v53 quad_perm:[2,3,0,1] row_mask:0xf bank_mask:0xf bound_ctrl:1
	v_pk_fma_f32 v[52:53], v[172:173], v[60:61], v[58:59]
	v_bfe_u32 v60, v54, 16, 1
	v_bfe_u32 v51, v53, 16, 1
	v_add3_u32 v54, v54, v60, s23
	v_bfe_u32 v60, v57, 16, 1
	v_bfe_u32 v59, v55, 16, 1
	v_add3_u32 v51, v53, v51, s23
	v_bfe_u32 v53, v26, 16, 1
	v_add3_u32 v57, v57, v60, s23
	v_add3_u32 v55, v55, v59, s23
	v_add3_u32 v26, v26, v53, s23
	v_lshrrev_b32_e32 v53, 16, v57
	v_and_or_b32 v53, v51, s95, v53
	v_mul_f32_e32 v51, 0x4b800000, v50
	v_cmp_gt_f32_e32 vcc, s66, v50
	v_cndmask_b32_e32 v50, v50, v51, vcc
	v_cvt_pk_bf16_f32 v52, v56, v52
	v_rsq_f32_e32 v56, v50
	v_lshrrev_b32_e32 v26, 16, v26
	v_cvt_pk_bf16_f32 v27, v27, 0
	v_and_or_b32 v50, v54, s95, v26
	v_mul_f32_e32 v26, 0x45800000, v56
	v_and_or_b32 v51, v55, s95, v27
	v_cndmask_b32_e32 v26, v56, v26, vcc
	global_store_dwordx4 v[216:217], v[50:53], off
	v_pk_mul_f32 v[54:55], v[26:27], v[76:77] op_sel_hi:[0,1]
	v_pk_mul_f32 v[54:55], v[36:37], v[54:55]
	v_pk_mul_f32 v[50:51], v[26:27], v[74:75] op_sel_hi:[0,1]
	v_pk_mul_f32 v[50:51], v[90:91], v[50:51]
	v_mov_b32_dpp v56, v54 quad_perm:[2,3,0,1] row_mask:0xf bank_mask:0xf bound_ctrl:1
	v_pk_mul_f32 v[58:59], v[70:71], v[50:51]
	v_mov_b32_dpp v52, v50 quad_perm:[2,3,0,1] row_mask:0xf bank_mask:0xf bound_ctrl:1
	v_mov_b32_dpp v53, v51 quad_perm:[2,3,0,1] row_mask:0xf bank_mask:0xf bound_ctrl:1
	v_pk_fma_f32 v[50:51], v[170:171], v[52:53], v[58:59]
	v_pk_mul_f32 v[52:53], v[176:177], v[54:55]
	v_mov_b32_dpp v57, v55 quad_perm:[2,3,0,1] row_mask:0xf bank_mask:0xf bound_ctrl:1
	v_pk_mul_f32 v[54:55], v[26:27], v[78:79] op_sel_hi:[0,1]
	v_pk_mul_f32 v[54:55], v[34:35], v[54:55]
	v_pk_mul_f32 v[26:27], v[26:27], v[80:81] op_sel_hi:[0,1]
	v_pk_fma_f32 v[52:53], v[168:169], v[56:57], v[52:53]
	v_mov_b32_dpp v56, v54 quad_perm:[2,3,0,1] row_mask:0xf bank_mask:0xf bound_ctrl:1
	v_pk_mul_f32 v[26:27], v[28:29], v[26:27]
	v_pk_mul_f32 v[60:61], v[66:67], v[54:55]
	v_mov_b32_dpp v57, v55 quad_perm:[2,3,0,1] row_mask:0xf bank_mask:0xf bound_ctrl:1
	v_mov_b32_dpp v58, v26 quad_perm:[2,3,0,1] row_mask:0xf bank_mask:0xf bound_ctrl:1
	v_pk_fma_f32 v[54:55], v[166:167], v[56:57], v[60:61]
	v_pk_mul_f32 v[56:57], v[174:175], v[26:27]
	v_mov_b32_dpp v59, v27 quad_perm:[2,3,0,1] row_mask:0xf bank_mask:0xf bound_ctrl:1
	v_pk_fma_f32 v[26:27], v[172:173], v[58:59], v[56:57]
	v_bfe_u32 v59, v52, 16, 1
	v_bfe_u32 v56, v27, 16, 1
	v_add3_u32 v74, v52, v59, s23
	v_add3_u32 v27, v27, v56, s23
	v_bfe_u32 v57, v26, 16, 1
	v_bfe_u32 v58, v53, 16, 1
	v_add3_u32 v26, v26, v57, s23
	v_cvt_pk_bf16_f32 v76, v50, 0
	v_cvt_pk_bf16_f32 v50, v54, 0
	v_add3_u32 v75, v53, v58, s23
	v_bfe_u32 v53, v51, 16, 1
	v_and_or_b32 v50, v26, s95, v50
	v_lshlrev_b32_e32 v26, 16, v46
	v_and_b32_e32 v46, 0xffff0000, v46
	v_lshlrev_b32_e32 v62, 16, v42
	v_and_b32_e32 v64, 0xffff0000, v42
	v_add3_u32 v51, v51, v53, s23
	v_mov_b32_e32 v52, v26
	v_mov_b32_e32 v53, v46
	v_lshlrev_b32_e32 v63, 16, v43
	v_and_b32_e32 v65, 0xffff0000, v43
	v_mov_b32_e32 v42, v62
	v_mov_b32_e32 v43, v64
	v_lshrrev_b32_e32 v77, 16, v51
	v_cvt_pk_bf16_f32 v51, v55, 0
; __device__ __forceinline__ unsigned pk2(float lo, float hi) { return f2bf(lo) | (f2bf(hi) << 16); }
; __device__ __forceinline__ float dpp_x1(float v) { return __builtin_bit_cast(float, __builtin_amdgcn_update_dpp(0, __builtin_bit_cast(int, v), 0xB1, 0xF, 0xF, true)); }
; __device__ __forceinline__ float dpp_x2(float v) { return __builtin_bit_cast(float, __builtin_amdgcn_update_dpp(0, __builtin_bit_cast(int, v), 0x4E, 0xF, 0xF, true)); }
; __device__ __forceinline__ float dpp_hm(float v) { return __builtin_bit_cast(float, __builtin_amdgcn_update_dpp(0, __builtin_bit_cast(int, v), 0x141, 0xF, 0xF, true)); }
; __device__ __forceinline__ void qk_vec(bf16_t* p, const u32x4 r, const float (&w)[8], const float (&cs)[8], const float (&sn)[8]) {
;     float x[8] = {bflo(r.x), bfhi(r.x), bflo(r.y), bfhi(r.y), bflo(r.z), bfhi(r.z), bflo(r.w), bfhi(r.w)};
;     float ss = 0.f;
; #pragma unroll
;     for (int e = 0; e < 8; ++e) ss += x[e] * x[e];
;     ss += dpp_x1(ss); ss += dpp_x2(ss); ss += dpp_hm(ss);
;     const float rstd = rsqrtf(ss * (1.f / 64.f) + NORM_EPS);
;     float o[8];
; #pragma unroll
;     for (int e = 0; e < 8; ++e) { const float y = x[e] * rstd * w[e]; o[e] = y * cs[e] + dpp_x2(y) * sn[e]; }
;     u32x4 q; q.x = pk2(o[0], o[1]); q.y = pk2(o[2], o[3]); q.z = pk2(o[4], o[5]); q.w = pk2(o[6], o[7]);
;     *(u32x4*)p = q;
; }
; __device__ __forceinline__ void prep_qk_rows4(KP Pk, Frame& F, int l, int row0) {
;     ...
;     for (int r = 0; r < 4; ++r) { bf16_t* up = U + (size_t)(row0 + r) * NU + 8 * F.lane;
;         qk_vec(up + UC_SQ, raw[r][0], wsq, cs[r], sn[r]); qk_vec(up + UC_DQ, raw[r][1], wdq, cs[r], sn[r]); qk_vec(up + UC_DK, raw[r][2], wdk, cs[r], sn[r]); }
;     qk_vec(U + (size_t)rowk * NU + UC_SK + 8 * (F.lane & 15), rawk, wsk, csk, snk);
	v_pk_mul_f32 v[52:53], v[52:53], v[52:53]
	v_pk_mul_f32 v[42:43], v[42:43], v[42:43]
	v_and_or_b32 v51, v27, s95, v51
	v_lshlrev_b32_e32 v27, 16, v47
	v_and_b32_e32 v47, 0xffff0000, v47
	v_mov_b32_e32 v66, v42
	v_mov_b32_e32 v67, v52
	v_mov_b32_e32 v52, v43
	v_mov_b32_e32 v54, v47
	v_mov_b32_e32 v55, v27
	v_pk_add_f32 v[42:43], v[66:67], v[52:53]
	v_mov_b32_e32 v52, v65
	v_mov_b32_e32 v53, v63
	v_pk_mul_f32 v[54:55], v[54:55], v[54:55]
	v_lshlrev_b32_e32 v56, 16, v48
	v_and_b32_e32 v58, 0xffff0000, v48
	v_pk_mul_f32 v[52:53], v[52:53], v[52:53]
	v_lshlrev_b32_e32 v66, 16, v44
	v_and_b32_e32 v68, 0xffff0000, v44
	v_lshlrev_b32_e32 v57, 16, v49
	v_and_b32_e32 v59, 0xffff0000, v49
	v_mov_b32_e32 v48, v58
	v_mov_b32_e32 v49, v56
	v_lshlrev_b32_e32 v67, 16, v45
	v_and_b32_e32 v69, 0xffff0000, v45
	v_mov_b32_e32 v44, v68
	v_mov_b32_e32 v45, v66
	v_mov_b32_e32 v72, v53
	v_mov_b32_e32 v73, v55
	v_pk_mul_f32 v[48:49], v[48:49], v[48:49]
	v_pk_mul_f32 v[44:45], v[44:45], v[44:45]
	v_pk_add_f32 v[42:43], v[72:73], v[42:43]
	v_mov_b32_e32 v53, v54
	v_mov_b32_e32 v60, v59
	v_mov_b32_e32 v61, v57
	v_mov_b32_e32 v70, v69
	v_mov_b32_e32 v71, v67
	v_pk_add_f32 v[42:43], v[52:53], v[42:43]
	v_mov_b32_e32 v52, v45
	v_mov_b32_e32 v53, v49
	v_pk_mul_f32 v[60:61], v[60:61], v[60:61]
	v_pk_mul_f32 v[70:71], v[70:71], v[70:71]
	v_pk_add_f32 v[42:43], v[52:53], v[42:43]
	v_mov_b32_e32 v45, v48
	v_pk_add_f32 v[42:43], v[44:45], v[42:43]
	v_mov_b32_e32 v44, v71
	v_mov_b32_e32 v45, v61
	v_pk_add_f32 v[42:43], v[44:45], v[42:43]
	v_mov_b32_e32 v71, v60
	v_pk_add_f32 v[42:43], v[70:71], v[42:43]
	v_and_or_b32 v49, v75, s95, v77
	v_and_or_b32 v48, v74, s95, v76
	v_mov_b32_dpp v45, v43 quad_perm:[1,0,3,2] row_mask:0xf bank_mask:0xf bound_ctrl:1
	v_mov_b32_dpp v44, v42 quad_perm:[1,0,3,2] row_mask:0xf bank_mask:0xf bound_ctrl:1
	v_pk_add_f32 v[42:43], v[42:43], v[44:45]
	global_store_dwordx4 v[192:193], v[48:51], off
	s_nop 0
	v_mov_b32_dpp v45, v43 quad_perm:[2,3,0,1] row_mask:0xf bank_mask:0xf bound_ctrl:1
	v_mov_b32_dpp v44, v42 quad_perm:[2,3,0,1] row_mask:0xf bank_mask:0xf bound_ctrl:1
	v_pk_add_f32 v[42:43], v[42:43], v[44:45]
	s_nop 1
	v_mov_b32_dpp v45, v43 row_half_mirror row_mask:0xf bank_mask:0xf bound_ctrl:1
	v_mov_b32_dpp v44, v42 row_half_mirror row_mask:0xf bank_mask:0xf bound_ctrl:1
	v_pk_add_f32 v[42:43], v[42:43], v[44:45]
	s_nop 0
	v_pk_fma_f32 v[42:43], v[42:43], s[8:9], v[92:93] op_sel_hi:[1,0,0]
	s_nop 0
	v_mul_f32_e32 v44, 0x4b800000, v43
	v_cmp_gt_f32_e32 vcc, s66, v43
	s_nop 1
	v_cndmask_b32_e32 v43, v43, v44, vcc
	v_rsq_f32_e32 v43, v43
	s_nop 0
	v_mul_f32_e32 v44, 0x45800000, v43
	v_cndmask_b32_e32 v44, v43, v44, vcc
	v_pk_mul_f32 v[26:27], v[44:45], v[26:27] op_sel_hi:[0,1]
	v_pk_mul_f32 v[26:27], v[98:99], v[26:27]
	v_pk_mul_f32 v[46:47], v[44:45], v[46:47] op_sel_hi:[0,1]
	v_pk_mul_f32 v[46:47], v[112:113], v[46:47]
	v_mov_b32_dpp v48, v26 quad_perm:[2,3,0,1] row_mask:0xf bank_mask:0xf bound_ctrl:1
	v_pk_mul_f32 v[52:53], v[10:11], v[26:27]
	v_mov_b32_dpp v49, v27 quad_perm:[2,3,0,1] row_mask:0xf bank_mask:0xf bound_ctrl:1
	v_mov_b32_dpp v50, v46 quad_perm:[2,3,0,1] row_mask:0xf bank_mask:0xf bound_ctrl:1
	v_pk_fma_f32 v[26:27], v[142:143], v[48:49], v[52:53]
	v_pk_mul_f32 v[48:49], v[150:151], v[46:47]
	v_mov_b32_dpp v51, v47 quad_perm:[2,3,0,1] row_mask:0xf bank_mask:0xf bound_ctrl:1
	v_pk_fma_f32 v[46:47], v[146:147], v[50:51], v[48:49]
	v_pk_mul_f32 v[48:49], v[44:45], v[56:57] op_sel_hi:[0,1]
	v_pk_mul_f32 v[48:49], v[110:111], v[48:49]
	v_pk_mul_f32 v[44:45], v[44:45], v[58:59] op_sel_hi:[0,1]
	v_pk_mul_f32 v[44:45], v[196:197], v[44:45]
	v_mov_b32_dpp v50, v48 quad_perm:[2,3,0,1] row_mask:0xf bank_mask:0xf bound_ctrl:1
	v_pk_mul_f32 v[54:55], v[6:7], v[48:49]
	v_mov_b32_dpp v51, v49 quad_perm:[2,3,0,1] row_mask:0xf bank_mask:0xf bound_ctrl:1
	v_mov_b32_dpp v52, v44 quad_perm:[2,3,0,1] row_mask:0xf bank_mask:0xf bound_ctrl:1
	v_pk_fma_f32 v[48:49], v[140:141], v[50:51], v[54:55]
	v_pk_mul_f32 v[50:51], v[148:149], v[44:45]
	v_mov_b32_dpp v53, v45 quad_perm:[2,3,0,1] row_mask:0xf bank_mask:0xf bound_ctrl:1
	v_pk_fma_f32 v[44:45], v[144:145], v[52:53], v[50:51]
	v_bfe_u32 v52, v46, 16, 1
	v_bfe_u32 v43, v45, 16, 1
	v_add3_u32 v46, v46, v52, s23
	v_bfe_u32 v51, v47, 16, 1
	v_add3_u32 v43, v45, v43, s23
	v_bfe_u32 v45, v26, 16, 1
	v_add3_u32 v47, v47, v51, s23
	v_add3_u32 v26, v26, v45, s23
	v_cvt_pk_bf16_f32 v45, v49, 0
	v_and_or_b32 v45, v43, s95, v45
	v_mul_f32_e32 v43, 0x4b800000, v42
	v_cmp_gt_f32_e32 vcc, s66, v42
	v_cndmask_b32_e32 v42, v42, v43, vcc
	v_cvt_pk_bf16_f32 v44, v48, v44
	v_rsq_f32_e32 v48, v42
	v_lshrrev_b32_e32 v26, 16, v26
	v_cvt_pk_bf16_f32 v27, v27, 0
	v_and_or_b32 v42, v46, s95, v26
	v_mul_f32_e32 v26, 0x45800000, v48
	v_and_or_b32 v43, v47, s95, v27
	v_cndmask_b32_e32 v26, v48, v26, vcc
	global_store_dwordx4 v[132:133], v[42:45], off offset:3072
	s_nop 1
	v_pk_mul_f32 v[42:43], v[26:27], v[62:63] op_sel_hi:[0,1]
	v_pk_mul_f32 v[20:21], v[20:21], v[42:43]
	v_pk_mul_f32 v[44:45], v[26:27], v[64:65] op_sel_hi:[0,1]
	v_pk_mul_f32 v[16:17], v[16:17], v[44:45]
	v_mov_b32_dpp v42, v20 quad_perm:[2,3,0,1] row_mask:0xf bank_mask:0xf bound_ctrl:1
	v_pk_mul_f32 v[46:47], v[10:11], v[20:21]
	v_mov_b32_dpp v43, v21 quad_perm:[2,3,0,1] row_mask:0xf bank_mask:0xf bound_ctrl:1
	v_mov_b32_dpp v44, v16 quad_perm:[2,3,0,1] row_mask:0xf bank_mask:0xf bound_ctrl:1
	v_pk_fma_f32 v[20:21], v[142:143], v[42:43], v[46:47]
	v_pk_mul_f32 v[42:43], v[150:151], v[16:17]
	v_mov_b32_dpp v45, v17 quad_perm:[2,3,0,1] row_mask:0xf bank_mask:0xf bound_ctrl:1
	v_pk_fma_f32 v[16:17], v[146:147], v[44:45], v[42:43]
	v_pk_mul_f32 v[42:43], v[26:27], v[66:67] op_sel_hi:[0,1]
; __device__ __forceinline__ unsigned pk2(float lo, float hi) { return f2bf(lo) | (f2bf(hi) << 16); }
; __device__ __forceinline__ float dpp_x1(float v) { return __builtin_bit_cast(float, __builtin_amdgcn_update_dpp(0, __builtin_bit_cast(int, v), 0xB1, 0xF, 0xF, true)); }
; __device__ __forceinline__ float dpp_x2(float v) { return __builtin_bit_cast(float, __builtin_amdgcn_update_dpp(0, __builtin_bit_cast(int, v), 0x4E, 0xF, 0xF, true)); }
; __device__ __forceinline__ float dpp_hm(float v) { return __builtin_bit_cast(float, __builtin_amdgcn_update_dpp(0, __builtin_bit_cast(int, v), 0x141, 0xF, 0xF, true)); }
; __device__ __forceinline__ void qk_vec(bf16_t* p, const u32x4 r, const float (&w)[8], const float (&cs)[8], const float (&sn)[8]) {
;     float x[8] = {bflo(r.x), bfhi(r.x), bflo(r.y), bfhi(r.y), bflo(r.z), bfhi(r.z), bflo(r.w), bfhi(r.w)};
;     float ss = 0.f;
; #pragma unroll
;     for (int e = 0; e < 8; ++e) ss += x[e] * x[e];
;     ss += dpp_x1(ss); ss += dpp_x2(ss); ss += dpp_hm(ss);
;     const float rstd = rsqrtf(ss * (1.f / 64.f) + NORM_EPS);
;     float o[8];
; #pragma unroll
;     for (int e = 0; e < 8; ++e) { const float y = x[e] * rstd * w[e]; o[e] = y * cs[e] + dpp_x2(y) * sn[e]; }
;     u32x4 q; q.x = pk2(o[0], o[1]); q.y = pk2(o[2], o[3]); q.z = pk2(o[4], o[5]); q.w = pk2(o[6], o[7]);
;     *(u32x4*)p = q;
; }
; __device__ __forceinline__ void prep_qk_rows4(KP Pk, Frame& F, int l, int row0) {
;     ...
;         qk_vec(up + UC_SQ, raw[r][0], wsq, cs[r], sn[r]); qk_vec(up + UC_DQ, raw[r][1], wdq, cs[r], sn[r]); qk_vec(up + UC_DK, raw[r][2], wdk, cs[r], sn[r]); }
;     qk_vec(U + (size_t)rowk * NU + UC_SK + 8 * (F.lane & 15), rawk, wsk, csk, snk);
	v_pk_mul_f32 v[12:13], v[12:13], v[42:43]
	v_pk_mul_f32 v[26:27], v[26:27], v[68:69] op_sel_hi:[0,1]
	v_pk_mul_f32 v[8:9], v[8:9], v[26:27]
	v_mov_b32_dpp v42, v12 quad_perm:[2,3,0,1] row_mask:0xf bank_mask:0xf bound_ctrl:1
	v_pk_mul_f32 v[44:45], v[6:7], v[12:13]
	v_mov_b32_dpp v43, v13 quad_perm:[2,3,0,1] row_mask:0xf bank_mask:0xf bound_ctrl:1
	v_mov_b32_dpp v26, v8 quad_perm:[2,3,0,1] row_mask:0xf bank_mask:0xf bound_ctrl:1
	v_pk_fma_f32 v[12:13], v[140:141], v[42:43], v[44:45]
	v_pk_mul_f32 v[42:43], v[148:149], v[8:9]
	v_mov_b32_dpp v27, v9 quad_perm:[2,3,0,1] row_mask:0xf bank_mask:0xf bound_ctrl:1
	v_pk_fma_f32 v[8:9], v[144:145], v[26:27], v[42:43]
	v_bfe_u32 v42, v17, 16, 1
	v_bfe_u32 v26, v9, 16, 1
	v_bfe_u32 v27, v8, 16, 1
	v_bfe_u32 v43, v16, 16, 1
	v_add3_u32 v16, v16, v43, s23
	v_add3_u32 v17, v17, v42, s23
	v_add3_u32 v8, v8, v27, s23
	v_add3_u32 v9, v9, v26, s23
	v_cvt_pk_bf16_f32 v20, v20, 0
	v_cvt_pk_bf16_f32 v21, v21, 0
	v_cvt_pk_bf16_f32 v12, v12, 0
	v_cvt_pk_bf16_f32 v13, v13, 0
	v_and_or_b32 v45, v9, s95, v13
	v_and_or_b32 v44, v8, s95, v12
	v_and_or_b32 v43, v17, s95, v21
	v_and_or_b32 v42, v16, s95, v20
	global_store_dwordx4 v[178:179], v[42:45], off
	v_lshlrev_b32_e32 v8, 16, v38
	v_and_b32_e32 v12, 0xffff0000, v38
	v_lshlrev_b32_e32 v44, 16, v30
	v_and_b32_e32 v30, 0xffff0000, v30
	v_mov_b32_e32 v16, v8
	v_mov_b32_e32 v17, v12
	v_mov_b32_e32 v46, v44
	v_mov_b32_e32 v47, v30
	v_lshlrev_b32_e32 v9, 16, v39
	v_and_b32_e32 v13, 0xffff0000, v39
	v_pk_mul_f32 v[16:17], v[16:17], v[16:17]
	v_lshlrev_b32_e32 v45, 16, v31
	v_and_b32_e32 v31, 0xffff0000, v31
	v_pk_mul_f32 v[46:47], v[46:47], v[46:47]
	v_mov_b32_e32 v20, v13
	v_mov_b32_e32 v21, v9
	v_mov_b32_e32 v48, v46
	v_mov_b32_e32 v49, v16
	v_mov_b32_e32 v16, v47
	v_mov_b32_e32 v46, v31
	v_mov_b32_e32 v47, v45
	v_pk_mul_f32 v[20:21], v[20:21], v[20:21]
	v_lshlrev_b32_e32 v26, 16, v40
	v_and_b32_e32 v38, 0xffff0000, v40
	v_pk_add_f32 v[16:17], v[48:49], v[16:17]
	v_pk_mul_f32 v[46:47], v[46:47], v[46:47]
	v_lshlrev_b32_e32 v48, 16, v32
	v_and_b32_e32 v32, 0xffff0000, v32
	v_lshlrev_b32_e32 v27, 16, v41
	v_and_b32_e32 v39, 0xffff0000, v41
	v_mov_b32_e32 v40, v38
	v_mov_b32_e32 v41, v26
	v_mov_b32_e32 v50, v32
	v_mov_b32_e32 v51, v48
	v_mov_b32_e32 v54, v47
	v_mov_b32_e32 v55, v21
	v_pk_mul_f32 v[40:41], v[40:41], v[40:41]
	v_lshlrev_b32_e32 v49, 16, v33
	v_and_b32_e32 v33, 0xffff0000, v33
	v_pk_mul_f32 v[50:51], v[50:51], v[50:51]
	v_pk_add_f32 v[16:17], v[54:55], v[16:17]
	v_mov_b32_e32 v47, v20
	v_mov_b32_e32 v42, v39
	v_mov_b32_e32 v43, v27
	v_mov_b32_e32 v52, v33
	v_mov_b32_e32 v53, v49
	v_pk_add_f32 v[16:17], v[46:47], v[16:17]
	v_mov_b32_e32 v20, v51
	v_mov_b32_e32 v21, v41
	v_pk_mul_f32 v[42:43], v[42:43], v[42:43]
	v_pk_mul_f32 v[52:53], v[52:53], v[52:53]
	v_pk_add_f32 v[16:17], v[20:21], v[16:17]
	v_mov_b32_e32 v51, v40
	v_pk_add_f32 v[16:17], v[50:51], v[16:17]
	v_mov_b32_e32 v20, v53
	v_mov_b32_e32 v21, v43
	v_pk_add_f32 v[16:17], v[20:21], v[16:17]
	v_mov_b32_e32 v53, v42
	v_pk_add_f32 v[16:17], v[52:53], v[16:17]
	s_nop 1
	v_mov_b32_dpp v21, v17 quad_perm:[1,0,3,2] row_mask:0xf bank_mask:0xf bound_ctrl:1
	v_mov_b32_dpp v20, v16 quad_perm:[1,0,3,2] row_mask:0xf bank_mask:0xf bound_ctrl:1
	v_pk_add_f32 v[16:17], v[16:17], v[20:21]
	s_nop 1
	v_mov_b32_dpp v21, v17 quad_perm:[2,3,0,1] row_mask:0xf bank_mask:0xf bound_ctrl:1
	v_mov_b32_dpp v20, v16 quad_perm:[2,3,0,1] row_mask:0xf bank_mask:0xf bound_ctrl:1
	v_pk_add_f32 v[16:17], v[16:17], v[20:21]
	s_nop 1
	v_mov_b32_dpp v21, v17 row_half_mirror row_mask:0xf bank_mask:0xf bound_ctrl:1
	v_mov_b32_dpp v20, v16 row_half_mirror row_mask:0xf bank_mask:0xf bound_ctrl:1
	v_pk_add_f32 v[16:17], v[16:17], v[20:21]
	v_mov_b32_e32 v21, v24
	v_pk_fma_f32 v[16:17], v[16:17], s[8:9], v[92:93] op_sel_hi:[1,0,0]
	v_mov_b32_e32 v24, v23
	v_mul_f32_e32 v20, 0x4b800000, v17
	v_cmp_gt_f32_e32 vcc, s66, v17
	s_mov_b64 s[8:9], 0
	s_nop 0
	v_cndmask_b32_e32 v17, v17, v20, vcc
	v_rsq_f32_e32 v17, v17
	v_mov_b32_e32 v20, v22
	v_mul_f32_e32 v22, 0x45800000, v17
	v_cndmask_b32_e32 v22, v17, v22, vcc
	v_pk_mul_f32 v[8:9], v[22:23], v[8:9] op_sel_hi:[0,1]
	v_pk_mul_f32 v[8:9], v[90:91], v[8:9]
	v_pk_mul_f32 v[12:13], v[22:23], v[12:13] op_sel_hi:[0,1]
; __device__ __forceinline__ unsigned pk2(float lo, float hi) { return f2bf(lo) | (f2bf(hi) << 16); }
; __device__ __forceinline__ float dpp_x1(float v) { return __builtin_bit_cast(float, __builtin_amdgcn_update_dpp(0, __builtin_bit_cast(int, v), 0xB1, 0xF, 0xF, true)); }
; __device__ __forceinline__ float dpp_x2(float v) { return __builtin_bit_cast(float, __builtin_amdgcn_update_dpp(0, __builtin_bit_cast(int, v), 0x4E, 0xF, 0xF, true)); }
; __device__ __forceinline__ float dpp_hm(float v) { return __builtin_bit_cast(float, __builtin_amdgcn_update_dpp(0, __builtin_bit_cast(int, v), 0x141, 0xF, 0xF, true)); }
; __device__ __forceinline__ void qk_vec(bf16_t* p, const u32x4 r, const float (&w)[8], const float (&cs)[8], const float (&sn)[8]) {
;     float x[8] = {bflo(r.x), bfhi(r.x), bflo(r.y), bfhi(r.y), bflo(r.z), bfhi(r.z), bflo(r.w), bfhi(r.w)};
;     float ss = 0.f;
; #pragma unroll
;     for (int e = 0; e < 8; ++e) ss += x[e] * x[e];
;     ss += dpp_x1(ss); ss += dpp_x2(ss); ss += dpp_hm(ss);
;     const float rstd = rsqrtf(ss * (1.f / 64.f) + NORM_EPS);
;     float o[8];
; #pragma unroll
;     for (int e = 0; e < 8; ++e) { const float y = x[e] * rstd * w[e]; o[e] = y * cs[e] + dpp_x2(y) * sn[e]; }
;     u32x4 q; q.x = pk2(o[0], o[1]); q.y = pk2(o[2], o[3]); q.z = pk2(o[4], o[5]); q.w = pk2(o[6], o[7]);
;     *(u32x4*)p = q;
; }
; __device__ __forceinline__ void prep_qk_rows4(KP Pk, Frame& F, int l, int row0) {
;     ...
;         qk_vec(up + UC_SQ, raw[r][0], wsq, cs[r], sn[r]); qk_vec(up + UC_DQ, raw[r][1], wdq, cs[r], sn[r]); qk_vec(up + UC_DK, raw[r][2], wdk, cs[r], sn[r]); }
;     qk_vec(U + (size_t)rowk * NU + UC_SK + 8 * (F.lane & 15), rawk, wsk, csk, snk);
	v_pk_mul_f32 v[12:13], v[36:37], v[12:13]
	v_mov_b32_dpp v40, v8 quad_perm:[2,3,0,1] row_mask:0xf bank_mask:0xf bound_ctrl:1
	v_pk_mul_f32 v[10:11], v[10:11], v[8:9]
	v_mov_b32_dpp v41, v9 quad_perm:[2,3,0,1] row_mask:0xf bank_mask:0xf bound_ctrl:1
	v_mov_b32_dpp v36, v12 quad_perm:[2,3,0,1] row_mask:0xf bank_mask:0xf bound_ctrl:1
	v_pk_fma_f32 v[8:9], v[142:143], v[40:41], v[10:11]
	v_pk_mul_f32 v[10:11], v[150:151], v[12:13]
	v_mov_b32_dpp v37, v13 quad_perm:[2,3,0,1] row_mask:0xf bank_mask:0xf bound_ctrl:1
	v_pk_mul_f32 v[12:13], v[22:23], v[26:27] op_sel_hi:[0,1]
	v_pk_mul_f32 v[22:23], v[22:23], v[38:39] op_sel_hi:[0,1]
	v_pk_mul_f32 v[12:13], v[34:35], v[12:13]
	v_pk_mul_f32 v[22:23], v[28:29], v[22:23]
	v_pk_fma_f32 v[10:11], v[146:147], v[36:37], v[10:11]
	v_mov_b32_dpp v26, v12 quad_perm:[2,3,0,1] row_mask:0xf bank_mask:0xf bound_ctrl:1
	v_mov_b32_dpp v28, v22 quad_perm:[2,3,0,1] row_mask:0xf bank_mask:0xf bound_ctrl:1
	v_pk_mul_f32 v[6:7], v[6:7], v[12:13]
	v_mov_b32_dpp v27, v13 quad_perm:[2,3,0,1] row_mask:0xf bank_mask:0xf bound_ctrl:1
	v_pk_mul_f32 v[12:13], v[148:149], v[22:23]
	v_mov_b32_dpp v29, v23 quad_perm:[2,3,0,1] row_mask:0xf bank_mask:0xf bound_ctrl:1
	v_pk_fma_f32 v[6:7], v[140:141], v[26:27], v[6:7]
	v_pk_fma_f32 v[12:13], v[144:145], v[28:29], v[12:13]
	v_bfe_u32 v23, v11, 16, 1
	v_bfe_u32 v17, v13, 16, 1
	v_add3_u32 v11, v11, v23, s23
	v_bfe_u32 v23, v6, 16, 1
	v_bfe_u32 v22, v12, 16, 1
	v_add3_u32 v13, v13, v17, s23
	v_add3_u32 v6, v6, v23, s23
	v_add3_u32 v12, v12, v22, s23
	v_lshrrev_b32_e32 v6, 16, v6
	v_cvt_pk_bf16_f32 v17, v8, 0
	v_and_or_b32 v8, v12, s95, v6
	v_mul_f32_e32 v6, 0x4b800000, v16
	v_cmp_gt_f32_e32 vcc, s66, v16
	v_bfe_u32 v26, v10, 16, 1
	v_add3_u32 v10, v10, v26, s23
	v_cndmask_b32_e32 v6, v16, v6, vcc
	v_bfe_u32 v26, v7, 16, 1
	v_rsq_f32_e32 v12, v6
	v_add3_u32 v7, v7, v26, s23
	v_cvt_pk_bf16_f32 v22, v9, 0
	v_lshrrev_b32_e32 v7, 16, v7
	v_and_or_b32 v9, v13, s95, v7
	v_and_or_b32 v7, v11, s95, v22
	v_and_or_b32 v6, v10, s95, v17
	global_store_dwordx4 v[164:165], v[6:9], off
	s_nop 1
	v_mul_f32_e32 v6, 0x45800000, v12
	v_cndmask_b32_e32 v6, v12, v6, vcc
	v_pk_mul_f32 v[8:9], v[6:7], v[44:45] op_sel_hi:[0,1]
	v_pk_mul_f32 v[8:9], v[20:21], v[8:9]
	v_pk_mul_f32 v[12:13], v[6:7], v[30:31] op_sel_hi:[0,1]
	v_pk_mul_f32 v[12:13], v[24:25], v[12:13]
	v_mov_b32_dpp v10, v8 quad_perm:[2,3,0,1] row_mask:0xf bank_mask:0xf bound_ctrl:1
	v_pk_mul_f32 v[18:19], v[18:19], v[8:9]
	v_mov_b32_dpp v11, v9 quad_perm:[2,3,0,1] row_mask:0xf bank_mask:0xf bound_ctrl:1
	v_mov_b32_dpp v16, v12 quad_perm:[2,3,0,1] row_mask:0xf bank_mask:0xf bound_ctrl:1
	v_pk_fma_f32 v[8:9], v[154:155], v[10:11], v[18:19]
	v_pk_mul_f32 v[10:11], v[138:139], v[12:13]
	v_mov_b32_dpp v17, v13 quad_perm:[2,3,0,1] row_mask:0xf bank_mask:0xf bound_ctrl:1
	v_pk_fma_f32 v[10:11], v[156:157], v[16:17], v[10:11]
	v_pk_mul_f32 v[12:13], v[6:7], v[48:49] op_sel_hi:[0,1]
	v_mov_b32_e32 v16, v2
	v_mov_b32_e32 v17, v4
	v_pk_mul_f32 v[6:7], v[6:7], v[32:33] op_sel_hi:[0,1]
	v_mov_b32_e32 v4, v3
	v_pk_mul_f32 v[12:13], v[16:17], v[12:13]
	v_pk_mul_f32 v[4:5], v[4:5], v[6:7]
	v_pk_mul_f32 v[14:15], v[14:15], v[12:13]
	v_mov_b32_dpp v2, v12 quad_perm:[2,3,0,1] row_mask:0xf bank_mask:0xf bound_ctrl:1
	v_mov_b32_dpp v6, v4 quad_perm:[2,3,0,1] row_mask:0xf bank_mask:0xf bound_ctrl:1
	v_mov_b32_dpp v3, v13 quad_perm:[2,3,0,1] row_mask:0xf bank_mask:0xf bound_ctrl:1
	v_pk_mul_f32 v[12:13], v[158:159], v[4:5]
	v_mov_b32_dpp v7, v5 quad_perm:[2,3,0,1] row_mask:0xf bank_mask:0xf bound_ctrl:1
	v_pk_fma_f32 v[4:5], v[136:137], v[6:7], v[12:13]
	v_pk_fma_f32 v[2:3], v[152:153], v[2:3], v[14:15]
	v_bfe_u32 v6, v5, 16, 1
	v_bfe_u32 v7, v4, 16, 1
	v_bfe_u32 v12, v11, 16, 1
	v_bfe_u32 v13, v10, 16, 1
	v_add3_u32 v10, v10, v13, s23
	v_add3_u32 v11, v11, v12, s23
	v_add3_u32 v4, v4, v7, s23
	v_add3_u32 v5, v5, v6, s23
	v_bfe_u32 v12, v2, 16, 1
	v_bfe_u32 v13, v3, 16, 1
	v_add3_u32 v3, v3, v13, s23
	v_add3_u32 v2, v2, v12, s23
	v_cvt_pk_bf16_f32 v6, v8, 0
	v_cvt_pk_bf16_f32 v7, v9, 0
	v_lshrrev_b32_e32 v2, 16, v2
	v_lshrrev_b32_e32 v3, 16, v3
	v_and_or_b32 v5, v5, s95, v3
	v_and_or_b32 v4, v4, s95, v2
	v_and_or_b32 v3, v11, s95, v7
	v_and_or_b32 v2, v10, s95, v6
	global_store_dwordx4 v[160:161], v[2:5], off

; #define LAS __attribute__((address_space(3)))
; __device__ __forceinline__ unsigned pk2(float lo, float hi) { return f2bf(lo) | (f2bf(hi) << 16); }
; #define MFMA16(a, b, c) __builtin_amdgcn_mfma_f32_16x16x32_bf16((a), (b), (c), 0, 0, 0)
; __device__ __forceinline__ void ph_hyena_filters(KP Pk, Frame& F, int u) {
;     ...
;             for (int tile = F.wave; tile < L / 16; tile += NWAVES) {
;                 const f32x4* hp = (const f32x4*)(h2 + (size_t)(16 * tile + r16) * 64 + 8 * kg);
;                 const f32x4 a0 = hp[0], a1 = hp[1], a2 = hp[8], a3 = hp[9];
;                 u32x4 p0, p1; p0.x = pk2(a0[0], a0[1]); p0.y = pk2(a0[2], a0[3]); p0.z = pk2(a1[0], a1[1]); p0.w = pk2(a1[2], a1[3]); p1.x = pk2(a2[0], a2[1]); p1.y = pk2(a2[2], a2[3]); p1.z = pk2(a3[0], a3[1]); p1.w = pk2(a3[2], a3[3]);
;                 f32x4 d = MFMA16(__builtin_bit_cast(bf16x8, p0), wb[0], ((f32x4){0.f, 0.f, 0.f, 0.f})); d = MFMA16(__builtin_bit_cast(bf16x8, p1), wb[1], d);
;                 const int t0 = 16 * tile + 4 * kg;
; #pragma unroll
;                 for (int i = 0; i < 4; ++i) { d[i] *= expf(-(float)(t0 + i) * rl * delta); s += fabsf(d[i]); }
;                 *(LAS f32x4*)(HR + r16 * HRS + t0) = d; }
.LBB0_594:
	global_load_dwordx4 v[10:13], v[16:17], off offset:-112
	global_load_dwordx4 v[46:49], v[16:17], off offset:-128
	global_load_dwordx4 v[50:53], v[16:17], off offset:16
	global_load_dwordx4 v[54:57], v[16:17], off
	s_add_i32 s35, s35, 8
	v_lshl_add_u64 v[16:17], v[16:17], 0, s[14:15]
	s_cmp_ge_u32 s35, s34
	s_waitcnt vmcnt(2)
	v_bfe_u32 v58, v46, 16, 1
	v_add3_u32 v46, v46, v58, s23
	v_bfe_u32 v58, v47, 16, 1
	v_lshrrev_b32_e32 v46, 16, v46
	v_add3_u32 v47, v47, v58, s23
	v_and_or_b32 v46, v47, s95, v46
	v_cvt_pk_bf16_f32 v47, v48, v49
	v_cvt_pk_bf16_f32 v48, v10, v11
	v_cvt_pk_bf16_f32 v49, v12, v13
	s_waitcnt vmcnt(0)
	v_cvt_pk_bf16_f32 v10, v54, v55
	v_cvt_pk_bf16_f32 v11, v56, v57
	v_cvt_pk_bf16_f32 v12, v50, v51
	v_cvt_pk_bf16_f32 v13, v52, v53
	v_mfma_f32_16x16x32_bf16 v[46:49], v[46:49], v[2:5], 0
	s_nop 0
	v_mfma_f32_16x16x32_bf16 v[10:13], v[10:13], v[6:9], v[46:49]
	s_nop 5
	v_cvt_f32_i32_e32 v46, v19
	v_mul_f32_e64 v46, v18, -v46
	v_mul_f32_e32 v46, v1, v46
	v_mul_f32_e32 v47, 0x3fb8aa3b, v46
	v_fma_f32 v48, v46, s10, -v47
	v_rndne_f32_e32 v49, v47
	v_fmac_f32_e32 v48, 0x32a5705f, v46
	v_sub_f32_e32 v47, v47, v49
	v_add_f32_e32 v47, v47, v48
	v_exp_f32_e32 v47, v47
	v_cvt_i32_f32_e32 v48, v49
	v_cmp_ngt_f32_e32 vcc, s11, v46
	v_ldexp_f32 v47, v47, v48
	s_nop 0
	v_cndmask_b32_e32 v47, 0, v47, vcc
	v_cmp_nlt_f32_e32 vcc, s12, v46
	s_nop 1
	v_cndmask_b32_e32 v46, v237, v47, vcc
	v_add_u32_e32 v47, 1, v19
	v_cvt_f32_i32_e32 v47, v47
	v_mul_f32_e64 v47, v18, -v47
	v_mul_f32_e32 v47, v1, v47
	v_mul_f32_e32 v48, 0x3fb8aa3b, v47
	v_fma_f32 v49, v47, s10, -v48
	v_rndne_f32_e32 v50, v48
	v_fmac_f32_e32 v49, 0x32a5705f, v47
	v_sub_f32_e32 v48, v48, v50
	v_add_f32_e32 v48, v48, v49
	v_exp_f32_e32 v48, v48
	v_cvt_i32_f32_e32 v49, v50
	v_cmp_ngt_f32_e32 vcc, s11, v47
	v_ldexp_f32 v48, v48, v49
	s_nop 0
	v_cndmask_b32_e32 v48, 0, v48, vcc
	v_cmp_nlt_f32_e32 vcc, s12, v47
	s_nop 1
	v_cndmask_b32_e32 v47, v237, v48, vcc
	v_pk_mul_f32 v[10:11], v[46:47], v[10:11]
	v_add_u32_e32 v46, 2, v19
	v_cvt_f32_i32_e32 v46, v46
	v_add_f32_e64 v45, v45, |v10|
	v_add_f32_e64 v45, |v11|, v45
	v_mul_f32_e64 v46, v18, -v46
	v_mul_f32_e32 v46, v1, v46
	v_mul_f32_e32 v47, 0x3fb8aa3b, v46
	v_fma_f32 v48, v46, s10, -v47
	v_rndne_f32_e32 v49, v47
	v_fmac_f32_e32 v48, 0x32a5705f, v46
	v_sub_f32_e32 v47, v47, v49
	v_add_f32_e32 v47, v47, v48
	v_exp_f32_e32 v47, v47
	v_cvt_i32_f32_e32 v48, v49
	v_cmp_ngt_f32_e32 vcc, s11, v46
	v_ldexp_f32 v47, v47, v48
	s_nop 0
	v_cndmask_b32_e32 v47, 0, v47, vcc
	v_cmp_nlt_f32_e32 vcc, s12, v46
	s_nop 1
	v_cndmask_b32_e32 v46, v237, v47, vcc
	v_add_u32_e32 v47, 3, v19
	v_cvt_f32_i32_e32 v47, v47
	v_add_u32_e32 v19, 0x80, v19
	v_mul_f32_e64 v47, v18, -v47
	v_mul_f32_e32 v47, v1, v47
	v_mul_f32_e32 v48, 0x3fb8aa3b, v47
	v_fma_f32 v49, v47, s10, -v48
	v_rndne_f32_e32 v50, v48
	v_fmac_f32_e32 v49, 0x32a5705f, v47
	v_sub_f32_e32 v48, v48, v50
	v_add_f32_e32 v48, v48, v49
	v_exp_f32_e32 v48, v48
	v_cvt_i32_f32_e32 v49, v50
	v_cmp_ngt_f32_e32 vcc, s11, v47
	v_ldexp_f32 v48, v48, v49
	s_nop 0
	v_cndmask_b32_e32 v48, 0, v48, vcc
	v_cmp_nlt_f32_e32 vcc, s12, v47
	s_nop 1
	v_cndmask_b32_e32 v47, v237, v48, vcc
	v_pk_mul_f32 v[12:13], v[12:13], v[46:47]
	ds_write_b128 v44, v[10:13]
	v_add_f32_e64 v45, |v12|, v45
	v_add_f32_e64 v45, |v13|, v45
	v_add_u32_e32 v44, 0x200, v44
	s_cbranch_scc0 .LBB0_594

; #define LAS __attribute__((address_space(3)))
; template <bool NEEDQ>
; __device__ __forceinline__ void gla_sub_load(Frame& F, int b, int h, int dir, int kidx0, GlaIn& in) {
;     unsigned char* ws = F.ws;
;     int lane_o = F.lane; asm volatile("" : "+v"(lane_o));
;     const int tau = lane_o & 15, dq = lane_o >> 4, row = keyrow(b, kidx0 + tau);
;     const f32x4* ag = (const f32x4*)((const float*)(ws + WS_AG) + (size_t)row * 32 + dir * 16);
; #pragma unroll
;     for (int r4 = 0; r4 < 4; ++r4) in.ag[r4] = ag[r4];
;     const bf16_t* U = (const bf16_t*)(ws + WS_U) + (size_t)row * NU;
;     in.kv = *(const u32x4*)(U + UC_GK + h * 32 + dq * 8);
;     if (NEEDQ) in.qv = *(const u32x4*)(U + UC_GQ + h * 32 + dq * 8);
;     in.v0 = *(const u32x4*)(U + UC_GV + h * 64 + dq * 16); in.v1 = *(const u32x4*)(U + UC_GV + h * 64 + dq * 16 + 8);
; }
; template <bool NEEDQ>
; __device__ __forceinline__ void gla_sub_prep(Frame& F, int dir, const GlaIn& in, LAS unsigned char* wl, float (&ltot)[8]) {
;     int lane_o = F.lane; asm volatile("" : "+v"(lane_o));
;     const int tau = lane_o & 15, dq = lane_o >> 4;
;     const LAS float* gw = (const LAS float*)(wl + GL_GW) + dq * 8; const LAS float* gb = (const LAS float*)(wl + GL_GB) + dq * 8;
;     const f32x4* ag = in.ag;
;     float x[8];
;     { const f32x4 b0 = *(const LAS f32x4*)gb, b1 = *(const LAS f32x4*)(gb + 4); x[0] = b0[0]; x[1] = b0[1]; x[2] = b0[2]; x[3] = b0[3]; x[4] = b1[0]; x[5] = b1[1]; x[6] = b1[2]; x[7] = b1[3]; }
; #pragma unroll
;     for (int r4 = 0; r4 < 4; ++r4) { const f32x4 av = ag[r4]; f32x4 wq[4][2];
; #pragma unroll
; __device__ __forceinline__ void gla_pass_b(KP Pk, Frame& F, int l, int b, int h, int c, LAS unsigned char* wl) {
;     ...
;         for (int st = 0; st < 4; ++st) { const int sb = dir == 0 ? st : 3 - st;
;             int lane_o = F.lane; asm volatile("" : "+v"(lane_o)); const int r16 = lane_o & 15, kg = lane_o >> 4;
; #pragma unroll
;             for (int db = 0; db < 2; ++db)
; #pragma unroll
;                 for (int nb = 0; nb < 4; ++nb) { u32x2 w; w.x = pk2(Sr[db][nb][0], Sr[db][nb][1]); w.y = pk2(Sr[db][nb][2], Sr[db][nb][3]); *(LAS u32x2*)(wl + GL_ST + ((16 * nb + r16) * 40 + 16 * db + 4 * kg) * 2) = w; }
;             { GlaIn in; gla_sub_load<true>(F, b, h, dir, 64 * c + 16 * sb, in); gla_sub_prep<true>(F, dir, in, wl, ltot); }
.LBB0_652:
	v_mov_b32_e32 v34, v176
	v_and_b32_e32 v1, 15, v34
	v_ashrrev_i32_e32 v144, 4, v34
	v_cvt_pk_bf16_f32 v34, v30, v31
	v_lshlrev_b32_e32 v145, 3, v144
	v_cvt_pk_bf16_f32 v35, v32, v33
	v_mul_u32_u24_e32 v36, 0x50, v1
	v_add3_u32 v44, s29, v145, v36
	v_cvt_pk_bf16_f32 v36, v26, v27
	v_cvt_pk_bf16_f32 v37, v28, v29
	v_cvt_pk_bf16_f32 v38, v22, v23
	v_cvt_pk_bf16_f32 v39, v24, v25
	v_cvt_pk_bf16_f32 v40, v14, v15
	v_cvt_pk_bf16_f32 v41, v16, v17
	v_cvt_pk_bf16_f32 v42, v18, v19
	v_cvt_pk_bf16_f32 v43, v20, v21
	v_add_u32_e32 v45, 0x1800, v44
	ds_write2_b64 v45, v[34:35], v[42:43] offset0:224 offset1:228
	v_cvt_pk_bf16_f32 v34, v10, v11
	v_cvt_pk_bf16_f32 v35, v12, v13
	v_add_u32_e32 v42, 0x2000, v44
	ds_write2_b64 v42, v[36:37], v[34:35] offset0:128 offset1:132
	v_cvt_pk_bf16_f32 v34, v6, v7
	v_cvt_pk_bf16_f32 v35, v8, v9
	v_add_u32_e32 v36, 0x2800, v44
	ds_write2_b64 v36, v[38:39], v[34:35] offset0:32 offset1:36
	s_and_b64 s[34:35], s[46:47], exec
	s_cselect_b32 s5, s60, s4
	v_cvt_pk_bf16_f32 v34, v2, v3
	s_lshl_b32 s5, s5, 4
	s_add_i32 s5, s5, s75
	s_cmpk_lt_u32 s5, 0x100
	v_cvt_pk_bf16_f32 v35, v4, v5
	s_cselect_b32 s37, s18, s19
	ds_write2_b64 v36, v[40:41], v[34:35] offset0:192 offset1:196
	v_mov_b32_e32 v40, v176
	s_add_i32 s34, s37, s5
	s_mov_b32 s45, s61
	v_and_or_b32 v34, v40, 15, s34
	v_ashrrev_i32_e32 v35, 31, v34
	v_lshlrev_b64 v[36:37], 7, v[34:35]
	v_lshl_add_u64 v[36:37], s[8:9], 0, v[36:37]
	global_load_dwordx4 v[54:57], v[36:37], off offset:48
	global_load_dwordx4 v[58:61], v[36:37], off offset:32
	global_load_dwordx4 v[150:153], v[36:37], off offset:16
	global_load_dwordx4 v[154:157], v[36:37], off
	v_mov_b64_e32 v[36:37], s[56:57]
	v_ashrrev_i32_e32 v38, 1, v40
	v_mad_i64_i32 v[34:35], s[34:35], v34, s30, v[36:37]
	v_and_b32_e32 v38, -8, v38
	v_lshl_add_u64 v[36:37], v[34:35], 0, s[44:45]
	v_ashrrev_i32_e32 v39, 31, v38
	v_lshl_add_u64 v[36:37], v[38:39], 1, v[36:37]
	global_load_dwordx4 v[46:49], v[36:37], off offset:512
	global_load_dwordx4 v[42:45], v[36:37], off
	s_mov_b32 s63, s61
	v_and_b32_e32 v36, -16, v40
	v_lshl_add_u64 v[34:35], v[34:35], 0, s[62:63]
	v_ashrrev_i32_e32 v37, 31, v36
	v_lshl_add_u64 v[34:35], v[36:37], 1, v[34:35]
	global_load_dwordx4 v[38:41], v[34:35], off offset:1024
	s_nop 0
	global_load_dwordx4 v[34:37], v[34:35], off offset:1040
	v_mov_b32_e32 v146, v176
	s_nop 0
	v_ashrrev_i32_e32 v147, 1, v146
	v_and_b32_e32 v148, -8, v147
	v_lshl_add_u32 v149, v148, 2, s29
	ds_read_b128 v[160:163], v149 offset:15360
	ds_read_b128 v[50:53], v149 offset:15376
	ds_read_b128 v[164:167], v149 offset:13312
	ds_read_b128 v[168:171], v149 offset:13328
	ds_read_b128 v[178:181], v149 offset:13440
	ds_read_b128 v[184:187], v149 offset:13456
	ds_read_b128 v[188:191], v149 offset:13568
	ds_read_b128 v[196:199], v149 offset:13584
	ds_read_b128 v[200:203], v149 offset:13696
	ds_read_b128 v[204:207], v149 offset:13712
	s_waitcnt vmcnt(4) lgkmcnt(7)
	v_fma_f32 v160, v154, v164, v160
	v_fma_f32 v161, v154, v165, v161
	v_fma_f32 v162, v154, v166, v162
	v_fmac_f32_e32 v163, v154, v167
	s_waitcnt lgkmcnt(6)
	v_fma_f32 v172, v154, v168, v50
	v_fma_f32 v51, v154, v169, v51
	v_fma_f32 v50, v154, v170, v52
	v_fmac_f32_e32 v53, v154, v171
	s_waitcnt lgkmcnt(5)
	v_fmac_f32_e32 v160, v155, v178
	v_fmac_f32_e32 v161, v155, v179
	v_fmac_f32_e32 v162, v155, v180
	v_fmac_f32_e32 v163, v155, v181
	s_waitcnt lgkmcnt(4)
	v_fmac_f32_e32 v51, v155, v185
	v_fmac_f32_e32 v50, v155, v186
	v_fmac_f32_e32 v53, v155, v187
	v_fmac_f32_e32 v172, v155, v184
	s_waitcnt lgkmcnt(3)
	v_fmac_f32_e32 v160, v156, v188
	v_fmac_f32_e32 v161, v156, v189
	v_fmac_f32_e32 v162, v156, v190
	v_fmac_f32_e32 v163, v156, v191
	s_waitcnt lgkmcnt(2)
	v_fmac_f32_e32 v51, v156, v197
	v_fmac_f32_e32 v50, v156, v198
	v_fmac_f32_e32 v53, v156, v199
	v_fmac_f32_e32 v172, v156, v196
	s_waitcnt lgkmcnt(1)
	v_fmac_f32_e32 v160, v157, v200
	v_fmac_f32_e32 v161, v157, v201
	v_fmac_f32_e32 v162, v157, v202
	v_fmac_f32_e32 v163, v157, v203
	s_waitcnt lgkmcnt(0)
	v_fmac_f32_e32 v51, v157, v205
	v_fmac_f32_e32 v50, v157, v206
	v_fmac_f32_e32 v53, v157, v207
	v_fmac_f32_e32 v172, v157, v204
	ds_read_b128 v[154:157], v149 offset:13824
	ds_read_b128 v[164:167], v149 offset:13840
	ds_read_b128 v[168:171], v149 offset:13952
	ds_read_b128 v[178:181], v149 offset:13968
	ds_read_b128 v[184:187], v149 offset:14080
	ds_read_b128 v[188:191], v149 offset:14096
	ds_read_b128 v[196:199], v149 offset:14208
	ds_read_b128 v[200:203], v149 offset:14224
	s_waitcnt lgkmcnt(7)
	v_fmac_f32_e32 v160, v150, v154
	s_waitcnt lgkmcnt(3)
	v_mov_b32_e32 v142, v184
	s_waitcnt lgkmcnt(1)
	v_mov_b32_e32 v143, v196
	v_fmac_f32_e32 v160, v151, v168
	v_pk_mul_f32 v[142:143], v[152:153], v[142:143]
	v_fmac_f32_e32 v161, v150, v155
	v_add_f32_e32 v52, v160, v142
	v_mov_b32_e32 v196, v185
	v_fmac_f32_e32 v161, v151, v169
	v_add_f32_e32 v52, v52, v143
	v_pk_mul_f32 v[142:143], v[152:153], v[196:197]
	v_fmac_f32_e32 v162, v150, v156
	v_add_f32_e32 v142, v161, v142
	v_add_f32_e32 v173, v142, v143
	v_mov_b32_e32 v142, v186
	v_mov_b32_e32 v143, v198
	v_fmac_f32_e32 v162, v151, v170
	v_pk_mul_f32 v[142:143], v[152:153], v[142:143]
	v_fmac_f32_e32 v163, v150, v157
	v_add_f32_e32 v142, v162, v142
	v_mov_b32_e32 v198, v187
	v_fmac_f32_e32 v163, v151, v171
	v_add_f32_e32 v175, v142, v143
	v_pk_mul_f32 v[142:143], v[152:153], v[198:199]
	v_fmac_f32_e32 v172, v150, v164
	v_add_f32_e32 v142, v163, v142
	v_add_f32_e32 v177, v142, v143
	v_mov_b32_e32 v142, v188
	s_waitcnt lgkmcnt(0)
; #define LAS __attribute__((address_space(3)))
; template <bool NEEDQ>
; __device__ __forceinline__ void gla_sub_prep(Frame& F, int dir, const GlaIn& in, LAS unsigned char* wl, float (&ltot)[8]) {
;     ...
;     const LAS float* gw = (const LAS float*)(wl + GL_GW) + dq * 8; const LAS float* gb = (const LAS float*)(wl + GL_GB) + dq * 8;
;     const f32x4* ag = in.ag;
;     float x[8];
;     { const f32x4 b0 = *(const LAS f32x4*)gb, b1 = *(const LAS f32x4*)(gb + 4); x[0] = b0[0]; x[1] = b0[1]; x[2] = b0[2]; x[3] = b0[3]; x[4] = b1[0]; x[5] = b1[1]; x[6] = b1[2]; x[7] = b1[3]; }
; #pragma unroll
;     for (int r4 = 0; r4 < 4; ++r4) { const f32x4 av = ag[r4]; f32x4 wq[4][2];
; #pragma unroll
;         for (int rr = 0; rr < 4; ++rr) { wq[rr][0] = *(const LAS f32x4*)(gw + (4 * r4 + rr) * 32); wq[rr][1] = *(const LAS f32x4*)(gw + (4 * r4 + rr) * 32 + 4); }
;         __builtin_amdgcn_sched_barrier(0);
; #pragma unroll
;         for (int rr = 0; rr < 4; ++rr) { const f32x4 w0 = wq[rr][0], w1 = wq[rr][1];
;             x[0] += av[rr] * w0[0]; x[1] += av[rr] * w0[1]; x[2] += av[rr] * w0[2]; x[3] += av[rr] * w0[3]; x[4] += av[rr] * w1[0]; x[5] += av[rr] * w1[1]; x[6] += av[rr] * w1[2]; x[7] += av[rr] * w1[3]; }
;         __builtin_amdgcn_sched_barrier(0); }
	v_mov_b32_e32 v143, v200
	v_fmac_f32_e32 v172, v151, v178
	v_pk_mul_f32 v[142:143], v[152:153], v[142:143]
	v_fmac_f32_e32 v51, v150, v165
	v_fmac_f32_e32 v50, v150, v166
	v_fmac_f32_e32 v53, v150, v167
	v_add_f32_e32 v142, v172, v142
	v_mov_b32_e32 v200, v189
	v_fmac_f32_e32 v51, v151, v179
	v_fmac_f32_e32 v50, v151, v180
	v_fmac_f32_e32 v53, v151, v181
	v_add_f32_e32 v172, v142, v143
	v_pk_mul_f32 v[142:143], v[152:153], v[200:201]
	v_fmac_f32_e32 v50, v152, v190
	v_fmac_f32_e32 v53, v152, v191
	v_add_f32_e32 v51, v51, v142
	v_add_f32_e32 v51, v51, v143
	v_fmac_f32_e32 v50, v153, v202
	v_fmac_f32_e32 v53, v153, v203
	ds_read_b128 v[150:153], v149 offset:14336
	ds_read_b128 v[154:157], v149 offset:14352
	ds_read_b128 v[160:163], v149 offset:14464
	ds_read_b128 v[164:167], v149 offset:14480
	ds_read_b128 v[168:171], v149 offset:14592
	ds_read_b128 v[178:181], v149 offset:14608
	ds_read_b128 v[184:187], v149 offset:14720
	ds_read_b128 v[188:191], v149 offset:14736
	s_waitcnt lgkmcnt(7)
	v_mov_b32_e32 v142, v150
	s_waitcnt lgkmcnt(5)
	v_mov_b32_e32 v143, v160
	v_pk_mul_f32 v[142:143], v[58:59], v[142:143]
	v_mov_b32_e32 v160, v151
	v_add_f32_e32 v52, v52, v142
	v_add_f32_e32 v52, v52, v143
	v_pk_mul_f32 v[142:143], v[58:59], v[160:161]
	v_fmac_f32_e32 v50, v58, v156
	v_add_f32_e32 v142, v173, v142
	v_add_f32_e32 v150, v142, v143
	v_mov_b32_e32 v142, v152
	v_mov_b32_e32 v143, v162
	v_pk_mul_f32 v[142:143], v[58:59], v[142:143]
	v_mov_b32_e32 v162, v153
	v_add_f32_e32 v142, v175, v142
	v_add_f32_e32 v151, v142, v143
	v_pk_mul_f32 v[142:143], v[58:59], v[162:163]
	v_fmac_f32_e32 v53, v58, v157
	v_add_f32_e32 v142, v177, v142
	v_add_f32_e32 v152, v142, v143
	v_mov_b32_e32 v142, v154
	s_waitcnt lgkmcnt(4)
	v_mov_b32_e32 v143, v164
	v_pk_mul_f32 v[142:143], v[58:59], v[142:143]
	v_mov_b32_e32 v164, v155
	v_add_f32_e32 v142, v172, v142
	v_add_f32_e32 v153, v142, v143
	v_pk_mul_f32 v[142:143], v[58:59], v[164:165]
	v_fmac_f32_e32 v50, v59, v166
	v_fmac_f32_e32 v53, v59, v167
	s_waitcnt lgkmcnt(3)
	v_mov_b32_e32 v58, v168
	s_waitcnt lgkmcnt(1)
	v_mov_b32_e32 v59, v184
	v_pk_mul_f32 v[58:59], v[60:61], v[58:59]
	v_mov_b32_e32 v184, v169
	v_add_f32_e32 v52, v52, v58
	v_add_f32_e32 v52, v52, v59
	v_pk_mul_f32 v[58:59], v[60:61], v[184:185]
	v_add_f32_e32 v51, v51, v142
	v_add_f32_e32 v58, v150, v58
	v_add_f32_e32 v172, v58, v59
	v_mov_b32_e32 v58, v170
	v_mov_b32_e32 v59, v186
	v_pk_mul_f32 v[58:59], v[60:61], v[58:59]
	v_mov_b32_e32 v186, v171
	v_add_f32_e32 v58, v151, v58
	v_add_f32_e32 v173, v58, v59
	v_pk_mul_f32 v[58:59], v[60:61], v[186:187]
	v_add_f32_e32 v51, v51, v143
	v_add_f32_e32 v58, v152, v58
	v_add_f32_e32 v175, v58, v59
	v_mov_b32_e32 v58, v178
	s_waitcnt lgkmcnt(0)
	v_mov_b32_e32 v59, v188
	v_pk_mul_f32 v[58:59], v[60:61], v[58:59]
	v_mov_b32_e32 v188, v179
	v_add_f32_e32 v58, v153, v58
	v_add_f32_e32 v177, v58, v59
	v_pk_mul_f32 v[58:59], v[60:61], v[188:189]
	v_fmac_f32_e32 v50, v60, v180
	v_fmac_f32_e32 v53, v60, v181
	v_add_f32_e32 v51, v51, v58
	v_add_f32_e32 v51, v51, v59
	v_fmac_f32_e32 v50, v61, v190
	v_fmac_f32_e32 v53, v61, v191
	ds_read_b128 v[58:61], v149 offset:14848
	ds_read_b128 v[150:153], v149 offset:14864
	ds_read_b128 v[154:157], v149 offset:14976
	ds_read_b128 v[160:163], v149 offset:14992
	ds_read_b128 v[164:167], v149 offset:15104
	ds_read_b128 v[168:171], v149 offset:15120
	ds_read_b128 v[178:181], v149 offset:15232
	ds_read_b128 v[184:187], v149 offset:15248
	s_waitcnt lgkmcnt(5)
	v_mov_b32_e32 v143, v154
	v_mov_b32_e32 v154, v59
	v_mov_b32_e32 v142, v58
	v_pk_mul_f32 v[58:59], v[54:55], v[154:155]
	v_pk_mul_f32 v[142:143], v[54:55], v[142:143]
	v_add_f32_e32 v58, v172, v58
	v_add_f32_e32 v52, v52, v142
	v_add_f32_e32 v142, v58, v59
	v_mov_b32_e32 v58, v60
	v_mov_b32_e32 v59, v156
	v_pk_mul_f32 v[58:59], v[54:55], v[58:59]
	v_mov_b32_e32 v156, v61
	v_add_f32_e32 v58, v173, v58
	v_add_f32_e32 v60, v58, v59
	v_pk_mul_f32 v[58:59], v[54:55], v[156:157]
	v_fmac_f32_e32 v50, v54, v152
	v_add_f32_e32 v58, v175, v58
	v_add_f32_e32 v61, v58, v59
	v_mov_b32_e32 v58, v150
	s_waitcnt lgkmcnt(4)
	v_mov_b32_e32 v59, v160
	v_pk_mul_f32 v[58:59], v[54:55], v[58:59]
	v_fmac_f32_e32 v53, v54, v153
	v_add_f32_e32 v58, v177, v58
	v_mov_b32_e32 v160, v151
	v_add_f32_e32 v52, v52, v143
	v_add_f32_e32 v143, v58, v59
	v_pk_mul_f32 v[58:59], v[54:55], v[160:161]
	v_fmac_f32_e32 v50, v55, v162
	v_fmac_f32_e32 v53, v55, v163
	s_waitcnt lgkmcnt(3)
	v_mov_b32_e32 v54, v164
	s_waitcnt lgkmcnt(1)
	v_mov_b32_e32 v55, v178
	v_pk_mul_f32 v[54:55], v[56:57], v[54:55]
	v_mov_b32_e32 v178, v165
	v_add_f32_e32 v52, v52, v54
	v_add_f32_e32 v52, v52, v55
	v_pk_mul_f32 v[54:55], v[56:57], v[178:179]
	v_add_f32_e32 v51, v51, v58
	v_add_f32_e32 v54, v142, v54
	v_add_f32_e32 v58, v54, v55
	v_mov_b32_e32 v54, v166
	v_mov_b32_e32 v55, v180
	v_pk_mul_f32 v[54:55], v[56:57], v[54:55]
	v_mov_b32_e32 v180, v167
	v_add_f32_e32 v54, v60, v54
	v_add_f32_e32 v51, v51, v59
	v_add_f32_e32 v59, v54, v55
	v_pk_mul_f32 v[54:55], v[56:57], v[180:181]
	v_fmac_f32_e32 v50, v56, v170
	v_add_f32_e32 v54, v61, v54
	v_add_f32_e32 v60, v54, v55
	v_mov_b32_e32 v54, v168
	s_waitcnt lgkmcnt(0)
; #define GLA_DPP(v, ctrl) __builtin_bit_cast(float, __builtin_amdgcn_update_dpp(0, __builtin_bit_cast(int, (v)), (ctrl), 0xF, 0xF, true))
; template <bool NEEDQ>
; __device__ __forceinline__ void gla_sub_prep(Frame& F, int dir, const GlaIn& in, LAS unsigned char* wl, float (&ltot)[8]) {
;     ...
;     for (int j = 0; j < 8; ++j) x[j] = (fminf(x[j], 0.f) - __logf(1.f + __expf(-fabsf(x[j])))) * (1.f / 16.f);
;     ...
;     float tot[8];
; #pragma unroll
;     for (int j = 0; j < 8; ++j) { float t = x[j]; t += GLA_DPP(t, 0xB1); t += GLA_DPP(t, 0x4E); t += GLA_DPP(t, 0x141); t += GLA_DPP(t, 0x140); tot[j] = t; ltot[j] += t; }
	v_mov_b32_e32 v55, v184
	v_pk_mul_f32 v[54:55], v[56:57], v[54:55]
	v_mov_b32_e32 v184, v169
	v_add_f32_e32 v54, v143, v54
	v_add_f32_e32 v61, v54, v55
	v_pk_mul_f32 v[54:55], v[56:57], v[184:185]
	v_fmac_f32_e32 v53, v56, v171
	v_add_f32_e32 v51, v51, v54
	v_add_f32_e32 v51, v51, v55
	v_fmac_f32_e32 v50, v57, v186
	v_fmac_f32_e32 v53, v57, v187
	v_mul_f32_e64 v54, |v52|, s68
	v_exp_f32_e32 v54, v54
	v_mul_f32_e64 v55, |v58|, s68
	v_exp_f32_e32 v55, v55
	s_mov_b64 s[34:35], -1
	v_add_f32_e32 v54, 1.0, v54
	v_cmp_gt_f32_e32 vcc, s66, v54
	s_nop 1
	v_cndmask_b32_e64 v56, 0, 32, vcc
	v_ldexp_f32 v54, v54, v56
	v_log_f32_e32 v56, v54
	v_min_f32_e32 v54, 0, v52
	v_add_f32_e32 v52, 1.0, v55
	v_mul_f32_e32 v55, 0x3f317217, v56
	v_fma_f32 v55, v56, s71, -v55
	v_fmac_f32_e32 v55, 0x3377d1cf, v56
	v_fmac_f32_e32 v55, 0x3f317217, v56
	v_cmp_lt_f32_e64 s[40:41], |v56|, s13
	s_nop 1
	v_cndmask_b32_e64 v55, v56, v55, s[40:41]
	v_cmp_gt_f32_e64 s[40:41], s66, v52
	s_nop 1
	v_cndmask_b32_e64 v56, 0, 32, s[40:41]
	v_ldexp_f32 v52, v52, v56
	v_log_f32_e32 v52, v52
	v_cndmask_b32_e32 v56, 0, v241, vcc
	v_sub_f32_e32 v56, v55, v56
	v_min_f32_e32 v55, 0, v58
	v_mul_f32_e32 v57, 0x3f317217, v52
	v_mul_f32_e64 v58, |v59|, s68
	v_fma_f32 v57, v52, s71, -v57
	v_exp_f32_e32 v58, v58
	v_fmac_f32_e32 v57, 0x3377d1cf, v52
	v_fmac_f32_e32 v57, 0x3f317217, v52
	v_cmp_lt_f32_e64 vcc, |v52|, s13
	s_nop 1
	v_cndmask_b32_e32 v52, v52, v57, vcc
	v_cndmask_b32_e64 v57, 0, v241, s[40:41]
	v_sub_f32_e32 v57, v52, v57
	v_add_f32_e32 v52, 1.0, v58
	v_cmp_gt_f32_e32 vcc, s66, v52
	v_pk_add_f32 v[54:55], v[54:55], v[56:57] neg_lo:[0,1] neg_hi:[0,1]
	v_min_f32_e32 v56, 0, v59
	v_cndmask_b32_e64 v58, 0, 32, vcc
	v_ldexp_f32 v52, v52, v58
	v_log_f32_e32 v52, v52
	v_mul_f32_e64 v58, |v60|, s68
	v_exp_f32_e32 v58, v58
	v_pk_mul_f32 v[54:55], v[54:55], s[28:29] op_sel_hi:[1,0]
	v_mul_f32_e32 v57, 0x3f317217, v52
	v_fma_f32 v57, v52, s71, -v57
	v_fmac_f32_e32 v57, 0x3377d1cf, v52
	v_fmac_f32_e32 v57, 0x3f317217, v52
	v_cmp_lt_f32_e64 s[40:41], |v52|, s13
	s_nop 1
	v_cndmask_b32_e64 v52, v52, v57, s[40:41]
	v_add_f32_e32 v57, 1.0, v58
	v_cmp_gt_f32_e64 s[40:41], s66, v57
	s_nop 1
	v_cndmask_b32_e64 v58, 0, 32, s[40:41]
	v_ldexp_f32 v57, v57, v58
	v_log_f32_e32 v59, v57
	v_cndmask_b32_e32 v57, 0, v241, vcc
	v_sub_f32_e32 v58, v52, v57
	v_min_f32_e32 v57, 0, v60
	v_mul_f32_e32 v52, 0x3f317217, v59
	v_mul_f32_e64 v60, |v61|, s68
	v_fma_f32 v52, v59, s71, -v52
	v_exp_f32_e32 v60, v60
	v_fmac_f32_e32 v52, 0x3377d1cf, v59
	v_fmac_f32_e32 v52, 0x3f317217, v59
	v_cmp_lt_f32_e64 vcc, |v59|, s13
	s_nop 1
	v_cndmask_b32_e32 v52, v59, v52, vcc
	v_cndmask_b32_e64 v59, 0, v241, s[40:41]
	v_sub_f32_e32 v59, v52, v59
	v_add_f32_e32 v52, 1.0, v60
	v_cmp_gt_f32_e32 vcc, s66, v52
	v_pk_add_f32 v[56:57], v[56:57], v[58:59] neg_lo:[0,1] neg_hi:[0,1]
	s_nop 0
	v_cndmask_b32_e64 v60, 0, 32, vcc
	v_ldexp_f32 v52, v52, v60
	v_log_f32_e32 v52, v52
	v_mul_f32_e64 v60, |v51|, s68
	v_pk_mul_f32 v[58:59], v[56:57], s[28:29] op_sel_hi:[1,0]
	v_exp_f32_e32 v60, v60
	v_mul_f32_e32 v57, 0x3f317217, v52
	v_fma_f32 v57, v52, s71, -v57
	v_fmac_f32_e32 v57, 0x3377d1cf, v52
	v_fmac_f32_e32 v57, 0x3f317217, v52
	v_cmp_lt_f32_e64 s[40:41], |v52|, s13
	v_min_f32_e32 v56, 0, v61
	s_nop 0
	v_cndmask_b32_e64 v52, v52, v57, s[40:41]
	v_add_f32_e32 v57, 1.0, v60
	v_cmp_gt_f32_e64 s[40:41], s66, v57
	s_nop 1
	v_cndmask_b32_e64 v60, 0, 32, s[40:41]
	v_ldexp_f32 v57, v57, v60
	v_log_f32_e32 v61, v57
	v_cndmask_b32_e32 v57, 0, v241, vcc
	v_sub_f32_e32 v60, v52, v57
	v_min_f32_e32 v57, 0, v51
	v_mul_f32_e32 v51, 0x3f317217, v61
	v_mul_f32_e64 v52, |v50|, s68
	v_fma_f32 v51, v61, s71, -v51
	v_exp_f32_e32 v52, v52
	v_fmac_f32_e32 v51, 0x3377d1cf, v61
	v_fmac_f32_e32 v51, 0x3f317217, v61
	v_cmp_lt_f32_e64 vcc, |v61|, s13
	v_min_f32_e32 v50, 0, v50
	s_nop 0
	v_cndmask_b32_e32 v51, v61, v51, vcc
	v_cndmask_b32_e64 v61, 0, v241, s[40:41]
	v_sub_f32_e32 v61, v51, v61
	v_add_f32_e32 v51, 1.0, v52
	v_cmp_gt_f32_e32 vcc, s66, v51
	v_pk_add_f32 v[56:57], v[56:57], v[60:61] neg_lo:[0,1] neg_hi:[0,1]
	s_nop 0
	v_cndmask_b32_e64 v52, 0, 32, vcc
	v_ldexp_f32 v51, v51, v52
	v_log_f32_e32 v51, v51
	v_pk_mul_f32 v[142:143], v[56:57], s[28:29] op_sel_hi:[1,0]
	v_mul_f32_e64 v56, |v53|, s68
	v_exp_f32_e32 v56, v56
	v_mul_f32_e32 v52, 0x3f317217, v51
	v_fma_f32 v52, v51, s71, -v52
	v_fmac_f32_e32 v52, 0x3377d1cf, v51
	v_fmac_f32_e32 v52, 0x3f317217, v51
	v_cmp_lt_f32_e64 s[40:41], |v51|, s13
	s_nop 1
	v_cndmask_b32_e64 v51, v51, v52, s[40:41]
	v_cndmask_b32_e32 v52, 0, v241, vcc
	v_sub_f32_e32 v51, v51, v52
	v_add_f32_e32 v52, 1.0, v56
	v_cmp_gt_f32_e32 vcc, s66, v52
	v_sub_f32_e32 v50, v50, v51
	v_min_f32_e32 v51, 0, v53
	v_cndmask_b32_e64 v56, 0, 32, vcc
	v_ldexp_f32 v52, v52, v56
	v_log_f32_e32 v52, v52
	v_add_f32_dpp v56, v55, v55 quad_perm:[1,0,3,2] row_mask:0xf bank_mask:0xf bound_ctrl:1
	v_mul_f32_e32 v160, 0x3d800000, v50
	v_mul_f32_e32 v53, 0x3f317217, v52
	v_add_f32_dpp v56, v56, v56 quad_perm:[2,3,0,1] row_mask:0xf bank_mask:0xf bound_ctrl:1
	v_fma_f32 v53, v52, s71, -v53
	v_fmac_f32_e32 v53, 0x3377d1cf, v52
	v_add_f32_dpp v150, v56, v56 row_half_mirror row_mask:0xf bank_mask:0xf bound_ctrl:1
	v_add_f32_dpp v56, v58, v58 quad_perm:[1,0,3,2] row_mask:0xf bank_mask:0xf bound_ctrl:1
	v_fmac_f32_e32 v53, 0x3f317217, v52
	v_cmp_lt_f32_e64 s[40:41], |v52|, s13
	v_add_f32_dpp v56, v56, v56 quad_perm:[2,3,0,1] row_mask:0xf bank_mask:0xf bound_ctrl:1
	v_mov_b32_dpp v151, v150 row_mirror row_mask:0xf bank_mask:0xf bound_ctrl:1
	v_cndmask_b32_e64 v52, v52, v53, s[40:41]
; #define GLA_DPP(v, ctrl) __builtin_bit_cast(float, __builtin_amdgcn_update_dpp(0, __builtin_bit_cast(int, (v)), (ctrl), 0xF, 0xF, true))
; template <bool NEEDQ>
; __device__ __forceinline__ void gla_sub_prep(Frame& F, int dir, const GlaIn& in, LAS unsigned char* wl, float (&ltot)[8]) {
;     ...
;     float tot[8];
; #pragma unroll
;     for (int j = 0; j < 8; ++j) { float t = x[j]; t += GLA_DPP(t, 0xB1); t += GLA_DPP(t, 0x4E); t += GLA_DPP(t, 0x141); t += GLA_DPP(t, 0x140); tot[j] = t; ltot[j] += t; }
;     if (dir == 0) {
; #pragma unroll
;         for (int j = 0; j < 8; ++j) { x[j] += GLA_DPP(x[j], 0x111); x[j] += GLA_DPP(x[j], 0x112); x[j] += GLA_DPP(x[j], 0x114); x[j] += GLA_DPP(x[j], 0x118); } }
;     else {
; #pragma unroll
;         for (int j = 0; j < 8; ++j) { x[j] += GLA_DPP(x[j], 0x101); x[j] += GLA_DPP(x[j], 0x102); x[j] += GLA_DPP(x[j], 0x104); x[j] += GLA_DPP(x[j], 0x108); } }
	v_add_f32_dpp v152, v56, v56 row_half_mirror row_mask:0xf bank_mask:0xf bound_ctrl:1
	v_add_f32_dpp v56, v59, v59 quad_perm:[1,0,3,2] row_mask:0xf bank_mask:0xf bound_ctrl:1
	v_cndmask_b32_e32 v53, 0, v241, vcc
	v_sub_f32_e32 v52, v52, v53
	v_add_f32_dpp v56, v56, v56 quad_perm:[2,3,0,1] row_mask:0xf bank_mask:0xf bound_ctrl:1
	v_sub_f32_e32 v51, v51, v52
	v_mul_f32_e32 v165, 0x3d800000, v51
	v_add_f32_dpp v154, v56, v56 row_half_mirror row_mask:0xf bank_mask:0xf bound_ctrl:1
	v_add_f32_dpp v56, v142, v142 quad_perm:[1,0,3,2] row_mask:0xf bank_mask:0xf bound_ctrl:1
	v_add_f32_dpp v52, v54, v54 quad_perm:[1,0,3,2] row_mask:0xf bank_mask:0xf bound_ctrl:1
	v_mov_b32_dpp v153, v152 row_mirror row_mask:0xf bank_mask:0xf bound_ctrl:1
	v_add_f32_dpp v56, v56, v56 quad_perm:[2,3,0,1] row_mask:0xf bank_mask:0xf bound_ctrl:1
	v_add_f32_dpp v52, v52, v52 quad_perm:[2,3,0,1] row_mask:0xf bank_mask:0xf bound_ctrl:1
	v_mov_b32_dpp v155, v154 row_mirror row_mask:0xf bank_mask:0xf bound_ctrl:1
	v_add_f32_dpp v156, v56, v56 row_half_mirror row_mask:0xf bank_mask:0xf bound_ctrl:1
	v_add_f32_dpp v56, v143, v143 quad_perm:[1,0,3,2] row_mask:0xf bank_mask:0xf bound_ctrl:1
	v_add_f32_dpp v52, v52, v52 row_half_mirror row_mask:0xf bank_mask:0xf bound_ctrl:1
	v_mov_b32_dpp v157, v156 row_mirror row_mask:0xf bank_mask:0xf bound_ctrl:1
	v_add_f32_dpp v56, v56, v56 quad_perm:[2,3,0,1] row_mask:0xf bank_mask:0xf bound_ctrl:1
	v_mov_b32_dpp v53, v52 row_mirror row_mask:0xf bank_mask:0xf bound_ctrl:1
	s_andn2_b64 vcc, exec, s[26:27]
	v_add_f32_dpp v161, v56, v56 row_half_mirror row_mask:0xf bank_mask:0xf bound_ctrl:1
	v_mov_b32_dpp v56, v160 quad_perm:[1,0,3,2] row_mask:0xf bank_mask:0xf bound_ctrl:1
	v_fmac_f32_e32 v56, 0x3d800000, v50
	v_mov_b32_dpp v162, v161 row_mirror row_mask:0xf bank_mask:0xf bound_ctrl:1
	s_nop 0
	v_add_f32_dpp v50, v56, v56 quad_perm:[2,3,0,1] row_mask:0xf bank_mask:0xf bound_ctrl:1
	s_nop 1
	v_add_f32_dpp v163, v50, v50 row_half_mirror row_mask:0xf bank_mask:0xf bound_ctrl:1
	v_mov_b32_dpp v50, v165 quad_perm:[1,0,3,2] row_mask:0xf bank_mask:0xf bound_ctrl:1
	v_fmac_f32_e32 v50, 0x3d800000, v51
	v_mov_b32_dpp v164, v163 row_mirror row_mask:0xf bank_mask:0xf bound_ctrl:1
	s_nop 0
	v_add_f32_dpp v50, v50, v50 quad_perm:[2,3,0,1] row_mask:0xf bank_mask:0xf bound_ctrl:1
	s_nop 1
	v_add_f32_dpp v166, v50, v50 row_half_mirror row_mask:0xf bank_mask:0xf bound_ctrl:1
	s_nop 1
	v_mov_b32_dpp v167, v166 row_mirror row_mask:0xf bank_mask:0xf bound_ctrl:1
	s_cbranch_vccnz .LBB0_654
	v_mov_b32_dpp v50, v54 row_shl:1 row_mask:0xf bank_mask:0xf bound_ctrl:1
	v_mov_b32_dpp v51, v55 row_shl:1 row_mask:0xf bank_mask:0xf bound_ctrl:1
	v_pk_add_f32 v[50:51], v[54:55], v[50:51]
	v_add_f32_dpp v149, v160, v160 row_shl:1 row_mask:0xf bank_mask:0xf bound_ctrl:1
	s_mov_b64 s[34:35], 0
	v_mov_b32_dpp v56, v50 row_shl:2 row_mask:0xf bank_mask:0xf bound_ctrl:1
	v_mov_b32_dpp v57, v51 row_shl:2 row_mask:0xf bank_mask:0xf bound_ctrl:1
	v_pk_add_f32 v[50:51], v[50:51], v[56:57]
	v_add_f32_dpp v149, v149, v149 row_shl:2 row_mask:0xf bank_mask:0xf bound_ctrl:1
	s_nop 0
	v_mov_b32_dpp v56, v50 row_shl:4 row_mask:0xf bank_mask:0xf bound_ctrl:1
	v_mov_b32_dpp v57, v51 row_shl:4 row_mask:0xf bank_mask:0xf bound_ctrl:1
	v_pk_add_f32 v[50:51], v[50:51], v[56:57]
	v_add_f32_dpp v149, v149, v149 row_shl:4 row_mask:0xf bank_mask:0xf bound_ctrl:1
	s_nop 0
	v_mov_b32_dpp v56, v50 row_shl:8 row_mask:0xf bank_mask:0xf bound_ctrl:1
	v_mov_b32_dpp v57, v51 row_shl:8 row_mask:0xf bank_mask:0xf bound_ctrl:1
	v_pk_add_f32 v[50:51], v[50:51], v[56:57]
	v_mov_b32_dpp v56, v58 row_shl:1 row_mask:0xf bank_mask:0xf bound_ctrl:1
	v_mov_b32_dpp v57, v59 row_shl:1 row_mask:0xf bank_mask:0xf bound_ctrl:1
	v_pk_add_f32 v[56:57], v[58:59], v[56:57]
	v_add_f32_dpp v149, v149, v149 row_shl:8 row_mask:0xf bank_mask:0xf bound_ctrl:1
	s_nop 0
	v_mov_b32_dpp v60, v56 row_shl:2 row_mask:0xf bank_mask:0xf bound_ctrl:1
	v_mov_b32_dpp v61, v57 row_shl:2 row_mask:0xf bank_mask:0xf bound_ctrl:1
	v_pk_add_f32 v[56:57], v[56:57], v[60:61]
	s_nop 1
	v_mov_b32_dpp v60, v56 row_shl:4 row_mask:0xf bank_mask:0xf bound_ctrl:1
	v_mov_b32_dpp v61, v57 row_shl:4 row_mask:0xf bank_mask:0xf bound_ctrl:1
	v_pk_add_f32 v[56:57], v[56:57], v[60:61]
	s_nop 1
	v_mov_b32_dpp v60, v56 row_shl:8 row_mask:0xf bank_mask:0xf bound_ctrl:1
	v_mov_b32_dpp v61, v57 row_shl:8 row_mask:0xf bank_mask:0xf bound_ctrl:1
	v_pk_add_f32 v[56:57], v[56:57], v[60:61]
	v_mov_b32_dpp v60, v142 row_shl:1 row_mask:0xf bank_mask:0xf bound_ctrl:1
	v_mov_b32_dpp v61, v143 row_shl:1 row_mask:0xf bank_mask:0xf bound_ctrl:1
	v_pk_add_f32 v[60:61], v[142:143], v[60:61]
	s_nop 1
	v_mov_b32_dpp v168, v60 row_shl:2 row_mask:0xf bank_mask:0xf bound_ctrl:1
	v_mov_b32_dpp v169, v61 row_shl:2 row_mask:0xf bank_mask:0xf bound_ctrl:1
	v_pk_add_f32 v[60:61], v[60:61], v[168:169]
	s_nop 1
	v_mov_b32_dpp v168, v60 row_shl:4 row_mask:0xf bank_mask:0xf bound_ctrl:1
	v_mov_b32_dpp v169, v61 row_shl:4 row_mask:0xf bank_mask:0xf bound_ctrl:1
	v_pk_add_f32 v[60:61], v[60:61], v[168:169]
	s_nop 1
	v_mov_b32_dpp v168, v60 row_shl:8 row_mask:0xf bank_mask:0xf bound_ctrl:1
	v_mov_b32_dpp v169, v61 row_shl:8 row_mask:0xf bank_mask:0xf bound_ctrl:1
	v_pk_add_f32 v[60:61], v[60:61], v[168:169]
	v_add_f32_dpp v168, v165, v165 row_shl:1 row_mask:0xf bank_mask:0xf bound_ctrl:1
	s_nop 1
	v_add_f32_dpp v168, v168, v168 row_shl:2 row_mask:0xf bank_mask:0xf bound_ctrl:1
	s_nop 1
	v_add_f32_dpp v168, v168, v168 row_shl:4 row_mask:0xf bank_mask:0xf bound_ctrl:1
	s_nop 1
	v_mov_b32_dpp v169, v168 row_shl:8 row_mask:0xf bank_mask:0xf bound_ctrl:1

; #define LAS __attribute__((address_space(3)))
; __device__ __forceinline__ unsigned pk2(float lo, float hi) { return f2bf(lo) | (f2bf(hi) << 16); }
; #define MFMA16(a, b, c) __builtin_amdgcn_mfma_f32_16x16x32_bf16((a), (b), (c), 0, 0, 0)
; template <bool NEEDQ>
; __device__ __forceinline__ void gla_sub_prep(Frame& F, int dir, const GlaIn& in, LAS unsigned char* wl, float (&ltot)[8]) {
;     ...
;     { const u32x4 v0 = in.v0, v1 = in.v1;
;       const unsigned vw[8] = {v0.x, v0.y, v0.z, v0.w, v1.x, v1.y, v1.z, v1.w};
; #pragma unroll
;       for (int j = 0; j < 8; ++j) { *(LAS unsigned short*)(wl + GL_VT + ((dq * 16 + 2 * j) * 24 + tau) * 2) = (unsigned short)(vw[j] & 0xffffu); *(LAS unsigned short*)(wl + GL_VT + ((dq * 16 + 2 * j + 1) * 24 + tau) * 2) = (unsigned short)(vw[j] >> 16); } }
; __device__ __forceinline__ void gla_pass_b(KP Pk, Frame& F, int l, int b, int h, int c, LAS unsigned char* wl) {
;     ...
;             const bf16x8 bq = *(const LAS bf16x8*)(wl + GL_QT + (r16 * 40 + 8 * kg) * 2);
;             { const bf16x8 ka = *(const LAS bf16x8*)(wl + GL_KT + (r16 * 40 + 8 * kg) * 2);
;               f32x4 p = MFMA16(ka, bq, ((f32x4){0.f, 0.f, 0.f, 0.f}));
; #pragma unroll
;               for (int i = 0; i < 4; ++i) { const int sidx = 4 * kg + i; const bool keep = dir == 0 ? (sidx <= r16) : (sidx >= r16); p[i] = keep ? p[i] : 0.f; }
;               u32x2 w; w.x = pk2(p[0], p[1]); w.y = pk2(p[2], p[3]); *(LAS u32x2*)(wl + GL_PT + (r16 * 24 + 4 * kg) * 2) = w; }
;             bf16x8 pb = *(const LAS bf16x8*)(wl + GL_PT + (r16 * 24 + 8 * (kg & 1)) * 2); if (kg >= 2) pb = zf;
;             f32x4 o[4];
; #pragma unroll
;             for (int nb = 0; nb < 4; ++nb) { const bf16x8 sa = *(const LAS bf16x8*)(wl + GL_ST + ((16 * nb + r16) * 40 + 8 * kg) * 2);
;                 bf16x8 va = *(const LAS bf16x8*)(wl + GL_VT + ((16 * nb + r16) * 24 + 8 * (kg & 1)) * 2); if (kg >= 2) va = zf;
;                 o[nb] = MFMA16(sa, bq, ((f32x4){0.f, 0.f, 0.f, 0.f})); o[nb] = MFMA16(va, pb, o[nb]); }
.LBB0_658:
	s_or_b64 exec, exec, s[34:35]
	v_and_b32_e32 v42, 0x1ffffff0, v146
	v_mul_lo_u32 v42, v42, 24
	v_or_b32_e32 v43, v42, v52
	v_lshl_add_u32 v43, v43, 1, s29
	s_waitcnt vmcnt(1)
	ds_write_b16 v43, v38 offset:4096
	v_or_b32_e32 v43, v46, v42
	v_lshl_add_u32 v43, v43, 1, s29
	ds_write_b16_d16_hi v43, v38 offset:4096
	v_or_b32_e32 v38, 48, v42
	v_or_b32_e32 v43, v38, v52
	v_add_u32_e32 v38, v38, v46
	v_lshl_add_u32 v43, v43, 1, s29
	v_lshl_add_u32 v38, v38, 1, s29
	ds_write_b16 v43, v39 offset:4096
	ds_write_b16_d16_hi v38, v39 offset:4096
	v_or_b32_e32 v38, 0x60, v42
	v_or_b32_e32 v39, v38, v52
	v_add_u32_e32 v38, v38, v46
	v_lshl_add_u32 v39, v39, 1, s29
	v_lshl_add_u32 v38, v38, 1, s29
	ds_write_b16 v39, v40 offset:4096
	ds_write_b16_d16_hi v38, v40 offset:4096
	v_add_u32_e32 v38, 0x90, v42
	v_or_b32_e32 v39, v38, v52
	v_add_u32_e32 v38, v38, v46
	v_lshl_add_u32 v39, v39, 1, s29
	v_lshl_add_u32 v38, v38, 1, s29
	ds_write_b16 v39, v41 offset:4096
	ds_write_b16_d16_hi v38, v41 offset:4096
	v_add_u32_e32 v38, 0xc0, v42
	v_or_b32_e32 v39, v38, v52
	v_or_b32_e32 v38, v38, v46
	v_lshl_add_u32 v39, v39, 1, s29
	v_lshl_add_u32 v38, v38, 1, s29
	s_waitcnt vmcnt(0)
	ds_write_b16 v39, v34 offset:4096
	ds_write_b16_d16_hi v38, v34 offset:4096
	v_add_u32_e32 v34, 0xf0, v42
	v_or_b32_e32 v38, v34, v52
	v_add_u32_e32 v34, v34, v46
	v_lshl_add_u32 v38, v38, 1, s29
	v_lshl_add_u32 v34, v34, 1, s29
	ds_write_b16 v38, v35 offset:4096
	ds_write_b16_d16_hi v34, v35 offset:4096
	v_add_u32_e32 v34, 0x120, v42
	v_or_b32_e32 v35, v34, v52
	v_add_u32_e32 v34, v34, v46
	v_lshl_add_u32 v35, v35, 1, s29
	v_lshl_add_u32 v34, v34, 1, s29
	v_lshlrev_b32_e32 v58, 2, v144
	ds_write_b16 v35, v36 offset:4096
	ds_write_b16_d16_hi v34, v36 offset:4096
	v_add_u32_e32 v34, 0x150, v42
	v_cmp_le_i32_e32 vcc, v58, v1
	v_or_b32_e32 v35, v34, v52
	v_add_u32_e32 v34, v34, v46
	v_cndmask_b32_e64 v38, 0, 1, vcc
	v_cmp_ge_i32_e32 vcc, v58, v1
	v_lshl_add_u32 v35, v35, 1, s29
	v_lshl_add_u32 v34, v34, 1, s29
	v_cndmask_b32_e64 v39, 0, 1, vcc
	ds_write_b16 v35, v37 offset:4096
	ds_write_b16_d16_hi v34, v37 offset:4096
	v_mad_u32_u24 v34, v1, 40, v145
	v_cndmask_b32_e64 v38, v39, v38, s[46:47]
	v_or_b32_e32 v39, 1, v58
	v_cmp_lt_i32_e32 vcc, v58, v1
	v_lshl_add_u32 v59, v34, 1, s29
	ds_read_b128 v[34:37], v59 offset:1280
	ds_read_b128 v[46:49], v59
	v_cndmask_b32_e64 v40, 0, 1, vcc
	v_cmp_ge_i32_e32 vcc, v39, v1
	s_waitcnt lgkmcnt(0)
	v_mfma_f32_16x16x32_bf16 v[34:37], v[34:37], v[46:49], 0
	v_cndmask_b32_e64 v39, 0, 1, vcc
	v_cndmask_b32_e64 v39, v39, v40, s[46:47]
	v_or_b32_e32 v40, 2, v58
	v_cmp_le_i32_e32 vcc, v40, v1
	v_and_b32_e32 v38, 1, v38
	v_and_b32_e32 v39, 1, v39
	v_cndmask_b32_e64 v41, 0, 1, vcc
	v_cmp_ge_i32_e32 vcc, v40, v1
	s_mov_b64 s[34:35], -1
	s_nop 0
	v_cndmask_b32_e64 v40, 0, 1, vcc
	v_cndmask_b32_e64 v40, v40, v41, s[46:47]
	v_or_b32_e32 v41, 3, v58
	v_cmp_le_i32_e32 vcc, v41, v1
	v_and_b32_e32 v40, 1, v40
	s_nop 0
	v_cndmask_b32_e64 v42, 0, 1, vcc
	v_cmp_ge_i32_e32 vcc, v41, v1
	s_nop 1
	v_cndmask_b32_e64 v41, 0, 1, vcc
	v_cmp_eq_u32_e32 vcc, 1, v38
	v_cndmask_b32_e64 v41, v41, v42, s[46:47]
	v_and_b32_e32 v41, 1, v41
	v_cndmask_b32_e32 v34, 0, v34, vcc
	v_cmp_eq_u32_e32 vcc, 1, v39
	v_cndmask_b32_e32 v35, 0, v35, vcc
	v_cmp_eq_u32_e32 vcc, 1, v40
	v_cvt_pk_bf16_f32 v34, v34, v35
	s_nop 0
	v_cndmask_b32_e32 v35, 0, v36, vcc
	v_cmp_eq_u32_e32 vcc, 1, v41
	v_cvt_pk_bf16_f32 v35, v35, 0
	v_cndmask_b32_e32 v36, 0, v37, vcc
	v_bfe_u32 v37, v36, 16, 1
	v_add3_u32 v36, v36, v37, s23
	v_and_or_b32 v35, v36, s95, v35
	v_mad_u32_u24 v36, v1, 24, v58
	v_lshl_add_u32 v36, v36, 1, s29
	ds_write_b64 v36, v[34:35] offset:7168
	v_and_b32_e32 v34, 8, v145
	v_mad_u32_u24 v34, v1, 24, v34
	v_lshl_add_u32 v60, v34, 1, s29
	ds_read_b128 v[34:37], v60 offset:7168
	ds_read_b128 v[38:41], v60 offset:4096
	ds_read_b128 v[42:45], v59 offset:7936
	v_cmp_lt_i32_e32 vcc, 1, v144
	ds_read_b128 v[54:57], v59 offset:9216
	ds_read_b128 v[142:145], v59 offset:11776
	s_waitcnt lgkmcnt(3)
	v_cndmask_b32_e64 v41, v41, 0, vcc
	v_cndmask_b32_e64 v40, v40, 0, vcc
	v_cndmask_b32_e64 v39, v39, 0, vcc
	v_cndmask_b32_e64 v38, v38, 0, vcc
	s_waitcnt lgkmcnt(2)
	v_mfma_f32_16x16x32_bf16 v[42:45], v[42:45], v[46:49], 0
	v_cndmask_b32_e64 v53, v37, 0, vcc
	v_cndmask_b32_e64 v52, v36, 0, vcc
	v_cndmask_b32_e64 v51, v35, 0, vcc
	v_cndmask_b32_e64 v50, v34, 0, vcc
	s_nop 1
	v_mfma_f32_16x16x32_bf16 v[34:37], v[38:41], v[50:53], v[42:45]
	ds_read_b128 v[38:41], v60 offset:4864
	s_waitcnt lgkmcnt(2)
	v_mfma_f32_16x16x32_bf16 v[42:45], v[54:57], v[46:49], 0
	ds_read_b128 v[54:57], v59 offset:10496
	s_waitcnt lgkmcnt(1)
	v_cndmask_b32_e64 v41, v41, 0, vcc
	v_cndmask_b32_e64 v40, v40, 0, vcc
	v_cndmask_b32_e64 v39, v39, 0, vcc
	v_cndmask_b32_e64 v38, v38, 0, vcc
	s_waitcnt lgkmcnt(0)
	v_mfma_f32_16x16x32_bf16 v[54:57], v[54:57], v[46:49], 0
	v_mfma_f32_16x16x32_bf16 v[38:41], v[38:41], v[50:53], v[42:45]
	s_nop 2
	ds_read_b128 v[42:45], v60 offset:5632
	v_mfma_f32_16x16x32_bf16 v[46:49], v[142:145], v[46:49], 0
	s_waitcnt lgkmcnt(0)
	v_cndmask_b32_e64 v45, v45, 0, vcc
	v_cndmask_b32_e64 v44, v44, 0, vcc
	v_cndmask_b32_e64 v43, v43, 0, vcc
	v_cndmask_b32_e64 v42, v42, 0, vcc
	s_nop 1
	v_mfma_f32_16x16x32_bf16 v[42:45], v[42:45], v[50:53], v[54:57]
	s_nop 2
	ds_read_b128 v[54:57], v60 offset:6400
	s_waitcnt lgkmcnt(0)
	v_cndmask_b32_e64 v57, v57, 0, vcc
	v_cndmask_b32_e64 v56, v56, 0, vcc
	v_cndmask_b32_e64 v55, v55, 0, vcc
	v_cndmask_b32_e64 v54, v54, 0, vcc
	s_and_b64 vcc, exec, s[26:27]
	s_nop 0
	v_mfma_f32_16x16x32_bf16 v[46:49], v[54:57], v[50:53], v[46:49]
	s_cbranch_vccnz .LBB0_661
	s_and_b64 vcc, exec, s[34:35]
	s_cbranch_vccnz .LBB0_671

; __device__ __forceinline__ unsigned pk2(float lo, float hi) { return f2bf(lo) | (f2bf(hi) << 16); }
; #define OF_PUT(k) { _Pragma("unroll") for (int nb = 0; nb < 4; ++nb) of[k][nb] = t[nb]; }
; __device__ __forceinline__ void gla_pass_b(KP Pk, Frame& F, int l, int b, int h, int c, LAS unsigned char* wl) {
;     ...
;             if (dir == 0) { u32x2 t[4];
; #pragma unroll
;                 for (int nb = 0; nb < 4; ++nb) { t[nb].x = pk2(o[nb][0], o[nb][1]); t[nb].y = pk2(o[nb][2], o[nb][3]); }
;     ...
;                 if (sb == 0) OF_PUT(0) else if (sb == 1) OF_PUT(1) else if (sb == 2) OF_PUT(2) else OF_PUT(3)
.LBB0_671:
	v_cvt_pk_bf16_f32 v34, v34, v35
	v_cvt_pk_bf16_f32 v35, v36, v37
	v_cvt_pk_bf16_f32 v36, v38, v39
	v_cvt_pk_bf16_f32 v37, v40, v41
	v_cvt_pk_bf16_f32 v38, v42, v43
	v_cvt_pk_bf16_f32 v39, v44, v45
	v_cvt_pk_bf16_f32 v42, v46, v47
	v_bfe_u32 v40, v49, 16, 1
	v_cvt_pk_bf16_f32 v1, v48, 0
	v_add3_u32 v40, v49, v40, s23
	v_and_or_b32 v43, v40, s95, v1
	s_cmp_lt_i32 s60, 1
	s_mov_b64 s[34:35], -1
	s_cbranch_scc1 .LBB0_679
	s_cmp_lt_i32 s60, 2
	s_cbranch_scc1 .LBB0_676
	s_cmp_lg_u32 s60, 2
	v_mov_b64_e32 v[40:41], v[140:141]
	v_mov_b64_e32 v[44:45], v[138:139]
	v_mov_b64_e32 v[46:47], v[136:137]
	v_mov_b64_e32 v[48:49], v[134:135]
	v_mov_b64_e32 v[50:51], v[34:35]
	v_mov_b64_e32 v[52:53], v[36:37]
	v_mov_b64_e32 v[54:55], v[38:39]
	v_mov_b64_e32 v[56:57], v[42:43]
	s_cbranch_scc0 .LBB0_675
	v_mov_b64_e32 v[40:41], v[42:43]
	v_mov_b64_e32 v[44:45], v[38:39]
	v_mov_b64_e32 v[46:47], v[36:37]
	v_mov_b64_e32 v[48:49], v[34:35]
	v_mov_b64_e32 v[50:51], v[124:125]
	v_mov_b64_e32 v[52:53], v[122:123]
	v_mov_b64_e32 v[54:55], v[120:121]
	v_mov_b64_e32 v[56:57], v[118:119]

; #define LAS __attribute__((address_space(3)))
; __device__ __forceinline__ unsigned pk2(float lo, float hi) { return f2bf(lo) | (f2bf(hi) << 16); }
; __device__ __forceinline__ unsigned pk2q(float lo, float hi) { return f2bf(q8(lo)) | (f2bf(q8(hi)) << 16); }
; #define LDS_WAIT() asm volatile("s_waitcnt lgkmcnt(0)" ::: "memory")
; __device__ __forceinline__ void p0_transpose_item(const float* W, int ldw, int srccol0, int k0, bf16_t* dst, int K, LAS float* scr, int lane, bool q = false) {
;     { f32x4 v[8];
; #pragma unroll
;       for (int i = 0; i < 8; ++i) v[i] = *(const f32x4*)(W + (size_t)(k0 + 8 * i + (lane >> 3)) * ldw + srccol0 + 4 * (lane & 7));
; #pragma unroll
;       for (int i = 0; i < 8; ++i) { LAS float* p = scr + (8 * i + (lane >> 3)) * 33 + 4 * (lane & 7); p[0] = v[i][0]; p[1] = v[i][1]; p[2] = v[i][2]; p[3] = v[i][3]; } }
;     LDS_WAIT(); asm volatile("" ::: "memory");
;     const int c = lane & 7;
; #pragma unroll
;     for (int j = 0; j < 4; ++j) { const int n = (lane >> 3) + 8 * j; const LAS float* s = scr + (8 * c) * 33 + n;
;         u32x4 o; if (q) { o.x = pk2q(s[0 * 33], s[1 * 33]); o.y = pk2q(s[2 * 33], s[3 * 33]); o.z = pk2q(s[4 * 33], s[5 * 33]); o.w = pk2q(s[6 * 33], s[7 * 33]); }
;         else { o.x = pk2(s[0 * 33], s[1 * 33]); o.y = pk2(s[2 * 33], s[3 * 33]); o.z = pk2(s[4 * 33], s[5 * 33]); o.w = pk2(s[6 * 33], s[7 * 33]); }
;         *(u32x4*)(dst + (size_t)n * K + k0 + 8 * c) = o; }
;     LDS_WAIT(); asm volatile("" ::: "memory");
; }
; __device__ __forceinline__ void p0_item(KP Pk, Frame& F, int it, LAS float* scr) {
;     ...
;         if (r < TI_WA) { if (WIN_F8_L(l)) p0_transpose_item8(Pk->in[I_WIN] + (size_t)l * D * DIN, DIN, 1536, 64 * r, ws + WS_WA + (size_t)l * 32 * D * 2, D, scr, F.lane);
;             else p0_transpose_item(Pk->in[I_WIN] + (size_t)l * D * DIN, DIN, 1536, 64 * r, (bf16_t*)(ws + WS_WA) + (size_t)l * 32 * D, D, scr, F.lane); return; }
.LBB0_847:
	s_andn2_b64 vcc, exec, s[34:35]
	s_cbranch_vccnz .LBB0_849
	s_ashr_i32 s19, s60, 31
	s_mul_i32 s9, s60, 0x2a40000
	s_mul_hi_i32 s5, s60, 0x2a40000
	s_waitcnt lgkmcnt(0)
	s_add_u32 s26, s26, s9
	s_addc_u32 s27, s27, s5
	v_lshlrev_b32_e32 v42, 2, v4
	v_mov_b32_e32 v43, v0
	v_lshl_add_u64 v[42:43], s[26:27], 0, v[42:43]
	s_mov_b64 s[26:27], 0x1800
	v_lshl_add_u64 v[64:65], v[42:43], 0, s[26:27]
	v_lshl_add_u64 v[36:37], v[64:65], 0, v[36:37]
	v_lshl_add_u64 v[34:35], v[64:65], 0, v[34:35]
	global_load_dwordx4 v[42:45], v[36:37], off
	v_lshl_add_u64 v[32:33], v[64:65], 0, v[32:33]
	global_load_dwordx4 v[34:37], v[34:35], off
	s_mov_b32 s18, s60
	global_load_dwordx4 v[46:49], v[32:33], off
	v_mad_i64_i32 v[32:33], s[26:27], v41, s2, v[64:65]
	global_load_dwordx4 v[52:55], v[32:33], off
	v_mad_i64_i32 v[32:33], s[26:27], v40, s2, v[64:65]
	global_load_dwordx4 v[56:59], v[32:33], off
	v_mad_i64_i32 v[32:33], s[26:27], v39, s2, v[64:65]
	global_load_dwordx4 v[60:63], v[32:33], off
	v_mad_i64_i32 v[32:33], s[26:27], v38, s2, v[64:65]
	global_load_dwordx4 v[38:41], v[32:33], off
	v_mad_i64_i32 v[32:33], s[26:27], v3, s2, v[64:65]
	global_load_dwordx4 v[64:67], v[32:33], off
	v_add_u32_e32 v3, v1, v5
	v_add_u32_e32 v32, 0x420, v3
	s_lshl_b64 s[18:19], s[18:19], 17
	v_readlane_b32 s5, v255, 13
	s_add_u32 s5, s5, s18
	v_readlane_b32 s9, v255, 14
	s_addc_u32 s18, s9, s19
	s_mov_b32 s9, s61
	s_lshl_b64 s[8:9], s[8:9], 1
	s_add_u32 s8, s5, s8
	s_addc_u32 s9, s18, s9
	v_mov_b32_e32 v33, v0
	s_waitcnt vmcnt(7)
	ds_write2_b32 v3, v42, v43 offset1:1
	ds_write2_b32 v3, v44, v45 offset0:2 offset1:3
	s_waitcnt vmcnt(6)
	ds_write2_b32 v32, v34, v35 offset1:1
	v_add_u32_e32 v32, 0x428, v3
	ds_write2_b32 v32, v36, v37 offset1:1
	v_add_u32_e32 v32, 0x840, v3
	s_waitcnt vmcnt(5)
	ds_write2_b32 v32, v46, v47 offset1:1
	v_add_u32_e32 v32, 0x848, v3
	ds_write2_b32 v32, v48, v49 offset1:1
	v_add_u32_e32 v32, 0xc60, v3
	s_waitcnt vmcnt(4)
	ds_write2_b32 v32, v52, v53 offset1:1
	v_add_u32_e32 v32, 0xc68, v3
	ds_write2_b32 v32, v54, v55 offset1:1
	v_add_u32_e32 v32, 0x1080, v3
	s_waitcnt vmcnt(3)
	ds_write2_b32 v32, v56, v57 offset1:1
	v_add_u32_e32 v32, 0x1088, v3
	ds_write2_b32 v32, v58, v59 offset1:1
	v_add_u32_e32 v32, 0x14a0, v3
	s_waitcnt vmcnt(2)
	ds_write2_b32 v32, v60, v61 offset1:1
	v_add_u32_e32 v32, 0x14a8, v3
	ds_write2_b32 v32, v62, v63 offset1:1
	v_add_u32_e32 v32, 0x18c0, v3
	s_waitcnt vmcnt(1)
	ds_write2_b32 v32, v38, v39 offset1:1
	v_add_u32_e32 v32, 0x18c8, v3
	ds_write2_b32 v32, v40, v41 offset1:1
	v_add_u32_e32 v32, 0x1ce0, v3
	v_add_u32_e32 v3, 0x1ce8, v3
	s_waitcnt vmcnt(0)
	ds_write2_b32 v32, v64, v65 offset1:1
	ds_write2_b32 v3, v66, v67 offset1:1
	s_waitcnt lgkmcnt(0)
	ds_read2_b32 v[38:39], v50 offset0:33 offset1:41
	ds_read2_b32 v[40:41], v50 offset1:8
	ds_read2_b32 v[42:43], v50 offset0:66 offset1:74
	ds_read2_b32 v[44:45], v50 offset0:99 offset1:107
	ds_read2_b32 v[46:47], v50 offset0:132 offset1:140
	ds_read2_b32 v[48:49], v50 offset0:165 offset1:173
	ds_read2_b32 v[52:53], v50 offset0:198 offset1:206
	ds_read2_b32 v[54:55], v50 offset0:231 offset1:239
	s_waitcnt lgkmcnt(7)
	s_waitcnt lgkmcnt(6)
	v_cvt_pk_bf16_f32 v34, v40, v38
	s_waitcnt lgkmcnt(5)
	s_waitcnt lgkmcnt(4)
	v_cvt_pk_bf16_f32 v35, v42, v44
	s_waitcnt lgkmcnt(3)
	s_waitcnt lgkmcnt(2)
	v_cvt_pk_bf16_f32 v36, v46, v48
	s_waitcnt lgkmcnt(1)
	v_lshlrev_b32_e32 v32, 1, v6
	s_waitcnt lgkmcnt(0)
	v_lshl_add_u64 v[32:33], s[8:9], 0, v[32:33]
	v_cvt_pk_bf16_f32 v37, v52, v54
	v_lshl_add_u64 v[56:57], v[32:33], 0, v[24:25]
	global_store_dwordx4 v[56:57], v[34:37], off
	v_cvt_pk_bf16_f32 v34, v41, v39
	v_cvt_pk_bf16_f32 v35, v43, v45
	v_cvt_pk_bf16_f32 v36, v47, v49
	v_cvt_pk_bf16_f32 v37, v53, v55
	v_lshl_add_u64 v[38:39], v[32:33], 0, v[26:27]
	global_store_dwordx4 v[38:39], v[34:37], off
	ds_read2_b32 v[38:39], v50 offset0:49 offset1:57
	ds_read2_b32 v[40:41], v50 offset0:16 offset1:24
	ds_read2_b32 v[42:43], v50 offset0:82 offset1:90
	ds_read2_b32 v[44:45], v50 offset0:115 offset1:123
	ds_read2_b32 v[46:47], v50 offset0:148 offset1:156
	ds_read2_b32 v[48:49], v50 offset0:181 offset1:189
	ds_read2_b32 v[52:53], v50 offset0:214 offset1:222
	ds_read2_b32 v[54:55], v50 offset0:247 offset1:255
	s_waitcnt lgkmcnt(7)
	s_waitcnt lgkmcnt(6)
	v_cvt_pk_bf16_f32 v34, v40, v38
	s_waitcnt lgkmcnt(5)
	s_waitcnt lgkmcnt(4)
	v_cvt_pk_bf16_f32 v35, v42, v44
	s_waitcnt lgkmcnt(3)
	s_waitcnt lgkmcnt(2)
	v_cvt_pk_bf16_f32 v36, v46, v48
	s_waitcnt lgkmcnt(1)
	s_waitcnt lgkmcnt(0)
	v_cvt_pk_bf16_f32 v37, v52, v54
	v_lshl_add_u64 v[56:57], v[32:33], 0, v[28:29]
	global_store_dwordx4 v[56:57], v[34:37], off
	v_cvt_pk_bf16_f32 v34, v41, v39
	v_cvt_pk_bf16_f32 v35, v43, v45
	v_cvt_pk_bf16_f32 v36, v47, v49
	v_bfe_u32 v37, v55, 16, 1
	v_cvt_pk_bf16_f32 v3, v53, 0
	v_add3_u32 v37, v55, v37, s23
	v_and_or_b32 v37, v37, s95, v3
	v_lshl_add_u64 v[32:33], v[32:33], 0, v[30:31]
	global_store_dwordx4 v[32:33], v[34:37], off
	s_waitcnt lgkmcnt(0)

; #define LAS __attribute__((address_space(3)))
; __device__ __forceinline__ unsigned pk2(float lo, float hi) { return f2bf(lo) | (f2bf(hi) << 16); }
; __device__ __forceinline__ unsigned pk2q(float lo, float hi) { return f2bf(q8(lo)) | (f2bf(q8(hi)) << 16); }
; #define LDS_WAIT() asm volatile("s_waitcnt lgkmcnt(0)" ::: "memory")
; __device__ __forceinline__ void p0_transpose_item(const float* W, int ldw, int srccol0, int k0, bf16_t* dst, int K, LAS float* scr, int lane, bool q = false) {
;     { f32x4 v[8];
; #pragma unroll
;       for (int i = 0; i < 8; ++i) v[i] = *(const f32x4*)(W + (size_t)(k0 + 8 * i + (lane >> 3)) * ldw + srccol0 + 4 * (lane & 7));
; #pragma unroll
;       for (int i = 0; i < 8; ++i) { LAS float* p = scr + (8 * i + (lane >> 3)) * 33 + 4 * (lane & 7); p[0] = v[i][0]; p[1] = v[i][1]; p[2] = v[i][2]; p[3] = v[i][3]; } }
;     LDS_WAIT(); asm volatile("" ::: "memory");
;     const int c = lane & 7;
; #pragma unroll
;     for (int j = 0; j < 4; ++j) { const int n = (lane >> 3) + 8 * j; const LAS float* s = scr + (8 * c) * 33 + n;
;         u32x4 o; if (q) { o.x = pk2q(s[0 * 33], s[1 * 33]); o.y = pk2q(s[2 * 33], s[3 * 33]); o.z = pk2q(s[4 * 33], s[5 * 33]); o.w = pk2q(s[6 * 33], s[7 * 33]); }
;         else { o.x = pk2(s[0 * 33], s[1 * 33]); o.y = pk2(s[2 * 33], s[3 * 33]); o.z = pk2(s[4 * 33], s[5 * 33]); o.w = pk2(s[6 * 33], s[7 * 33]); }
;         *(u32x4*)(dst + (size_t)n * K + k0 + 8 * c) = o; }
;     LDS_WAIT(); asm volatile("" ::: "memory");
; }
; __device__ __forceinline__ void p0_item(KP Pk, Frame& F, int it, LAS float* scr) {
;     ...
;         if (r < TI_WIN) { const int kb = r / 168, nb = r % 168, n0 = 32 * nb;
;             if (WIN_F8_L(l)) p0_transpose_item8(Pk->in[I_WIN] + (size_t)l * D * DIN, DIN, n0 < 1536 ? n0 : n0 + 32, 64 * kb, ws + WS_WIN + (size_t)l * NU * D * 2 + (size_t)n0 * D, D, scr, F.lane);
;             else p0_transpose_item(Pk->in[I_WIN] + (size_t)l * D * DIN, DIN, n0 < 1536 ? n0 : n0 + 32, 64 * kb, (bf16_t*)(ws + WS_WIN) + ((size_t)l * NU + n0) * D, D, scr, F.lane); return; }
.LBB0_853:
	s_andn2_b64 vcc, exec, s[40:41]
	s_cbranch_vccnz .LBB0_819
	s_mul_hi_i32 s5, s60, 0x2a40000
	s_waitcnt lgkmcnt(0)
	s_add_u32 s9, s38, s4
	s_addc_u32 s18, s39, s5
	s_mul_i32 s4, s60, 0x1500
	s_ashr_i32 s19, s34, 31
	s_mul_hi_i32 s5, s60, 0x1500
	s_add_u32 s4, s4, s34
	s_addc_u32 s5, s5, s19
	s_lshl_b64 s[4:5], s[4:5], 12
	v_readlane_b32 s19, v255, 15
	s_add_u32 s19, s19, s4
	v_readlane_b32 s4, v255, 16
	s_addc_u32 s34, s4, s5
	s_lshl_b64 s[4:5], s[26:27], 2
	s_add_u32 s4, s9, s4
	s_addc_u32 s5, s18, s5
	v_mov_b32_e32 v37, v0
	v_lshl_add_u64 v[78:79], s[4:5], 0, v[36:37]
	v_lshl_add_u64 v[34:35], v[78:79], 0, v[34:35]
	global_load_dwordx4 v[34:37], v[34:35], off
	v_lshl_add_u64 v[32:33], v[78:79], 0, v[32:33]
	global_load_dwordx4 v[38:41], v[32:33], off
	v_mad_i64_i32 v[32:33], s[4:5], v62, s2, v[78:79]
	global_load_dwordx4 v[62:65], v[32:33], off
	v_mad_i64_i32 v[32:33], s[4:5], v61, s2, v[78:79]
	global_load_dwordx4 v[66:69], v[32:33], off
	v_mad_i64_i32 v[32:33], s[4:5], v60, s2, v[78:79]
	global_load_dwordx4 v[70:73], v[32:33], off
	v_mad_i64_i32 v[32:33], s[4:5], v59, s2, v[78:79]
	global_load_dwordx4 v[74:77], v[32:33], off
	v_mad_i64_i32 v[32:33], s[4:5], v58, s2, v[78:79]
	global_load_dwordx4 v[58:61], v[32:33], off
	v_mad_i64_i32 v[32:33], s[4:5], v57, s2, v[78:79]
	global_load_dwordx4 v[78:81], v[32:33], off
	s_ashr_i32 s9, s8, 31
	s_lshl_b64 s[4:5], s[8:9], 1
	s_add_u32 s8, s19, s4
	s_addc_u32 s9, s34, s5
	v_lshlrev_b32_e32 v32, 1, v6
	v_mov_b32_e32 v33, v0
	v_lshl_add_u64 v[32:33], s[8:9], 0, v[32:33]
	s_waitcnt vmcnt(7)
	ds_write2_b32 v3, v34, v35 offset1:1
	ds_write2_b32 v3, v36, v37 offset0:2 offset1:3
	s_waitcnt vmcnt(6)
	ds_write2_b32 v42, v38, v39 offset1:1
	ds_write2_b32 v43, v40, v41 offset1:1
	s_waitcnt vmcnt(5)
	ds_write2_b32 v44, v62, v63 offset1:1
	ds_write2_b32 v45, v64, v65 offset1:1
	s_waitcnt vmcnt(4)
	ds_write2_b32 v46, v66, v67 offset1:1
	ds_write2_b32 v47, v68, v69 offset1:1
	s_waitcnt vmcnt(3)
	ds_write2_b32 v48, v70, v71 offset1:1
	ds_write2_b32 v49, v72, v73 offset1:1
	s_waitcnt vmcnt(2)
	ds_write2_b32 v51, v74, v75 offset1:1
	ds_write2_b32 v52, v76, v77 offset1:1
	s_waitcnt vmcnt(1)
	ds_write2_b32 v53, v58, v59 offset1:1
	ds_write2_b32 v54, v60, v61 offset1:1
	s_waitcnt vmcnt(0)
	ds_write2_b32 v55, v78, v79 offset1:1
	ds_write2_b32 v56, v80, v81 offset1:1
	s_waitcnt lgkmcnt(0)
	ds_read2_b32 v[46:47], v50 offset0:33 offset1:41
	ds_read2_b32 v[48:49], v50 offset1:8
	v_lshl_add_u64 v[56:57], v[32:33], 0, v[24:25]
	s_waitcnt lgkmcnt(1)
	s_waitcnt lgkmcnt(0)
	v_cvt_pk_bf16_f32 v52, v48, v46
	ds_read2_b32 v[36:37], v50 offset0:66 offset1:74
	ds_read2_b32 v[34:35], v50 offset0:99 offset1:107
	ds_read2_b32 v[40:41], v50 offset0:132 offset1:140
	ds_read2_b32 v[38:39], v50 offset0:165 offset1:173
	ds_read2_b32 v[44:45], v50 offset0:198 offset1:206
	ds_read2_b32 v[42:43], v50 offset0:231 offset1:239
	s_waitcnt lgkmcnt(5)
	s_waitcnt lgkmcnt(4)
	v_cvt_pk_bf16_f32 v53, v36, v34
	s_waitcnt lgkmcnt(3)
	s_waitcnt lgkmcnt(2)
	v_cvt_pk_bf16_f32 v54, v40, v38
	s_waitcnt lgkmcnt(1)
	s_waitcnt lgkmcnt(0)
	v_cvt_pk_bf16_f32 v55, v44, v42
	v_cvt_pk_bf16_f32 v34, v49, v47
	v_cvt_pk_bf16_f32 v35, v37, v35
	v_cvt_pk_bf16_f32 v36, v41, v39
	v_cvt_pk_bf16_f32 v37, v45, v43
	v_lshl_add_u64 v[38:39], v[32:33], 0, v[26:27]
	global_store_dwordx4 v[56:57], v[52:55], off
	global_store_dwordx4 v[38:39], v[34:37], off
	ds_read2_b32 v[38:39], v50 offset0:49 offset1:57
	ds_read2_b32 v[40:41], v50 offset0:16 offset1:24
	ds_read2_b32 v[42:43], v50 offset0:82 offset1:90
	ds_read2_b32 v[44:45], v50 offset0:115 offset1:123
	ds_read2_b32 v[46:47], v50 offset0:148 offset1:156
	ds_read2_b32 v[48:49], v50 offset0:181 offset1:189
	ds_read2_b32 v[52:53], v50 offset0:214 offset1:222
	ds_read2_b32 v[54:55], v50 offset0:247 offset1:255
	s_waitcnt lgkmcnt(7)
	s_waitcnt lgkmcnt(6)
	v_cvt_pk_bf16_f32 v34, v40, v38
	s_waitcnt lgkmcnt(5)
	s_waitcnt lgkmcnt(4)
	v_cvt_pk_bf16_f32 v35, v42, v44
	s_waitcnt lgkmcnt(3)
	s_waitcnt lgkmcnt(2)
	v_cvt_pk_bf16_f32 v36, v46, v48
	s_waitcnt lgkmcnt(1)
	s_waitcnt lgkmcnt(0)
	v_cvt_pk_bf16_f32 v37, v52, v54
	v_lshl_add_u64 v[56:57], v[32:33], 0, v[28:29]
	global_store_dwordx4 v[56:57], v[34:37], off
	v_cvt_pk_bf16_f32 v34, v41, v39
	v_cvt_pk_bf16_f32 v35, v43, v45
	v_cvt_pk_bf16_f32 v36, v47, v49
	v_bfe_u32 v37, v55, 16, 1
	v_cvt_pk_bf16_f32 v3, v53, 0
	v_add3_u32 v37, v55, v37, s23
	v_and_or_b32 v37, v37, s95, v3
	v_lshl_add_u64 v[32:33], v[32:33], 0, v[30:31]
	global_store_dwordx4 v[32:33], v[34:37], off
	s_waitcnt lgkmcnt(0)
	s_branch .LBB0_819
